# baseline (speedup 1.0000x reference)
_Z10ode_kernelPKfPKDF16_S2_PfPKi:
	v_lshrrev_b32_e32 v167, 6, v0
	s_lshr_b32 s3, s2, 3
	v_add_u32_e32 v2, s3, v167
	s_load_dwordx4 s[4:7], s[0:1], 0x0
	s_load_dwordx2 s[12:13], s[0:1], 0x10
	v_and_b32_e32 v130, 3, v2
	v_and_b32_e32 v1, 63, v0
	v_readfirstlane_b32 s3, v130
	v_lshlrev_b32_e32 v166, 4, v1
	s_lshl_b32 s11, s3, 14
	v_lshl_or_b32 v2, v130, 17, v166
	v_mov_b32_e32 v3, 0
	s_and_b32 s17, s11, 0xc000
	s_mov_b32 s9, 0
	s_waitcnt lgkmcnt(0)
	v_lshl_add_u64 v[74:75], s[6:7], 0, v[2:3]
	s_lshl_b32 s8, s17, 1
	v_lshl_add_u64 v[46:47], v[74:75], 0, s[8:9]
	s_movk_i32 s15, 0x1000
	v_add_co_u32_e32 v18, vcc, s15, v46
	s_movk_i32 s14, 0x3000
	s_nop 0
	v_addc_co_u32_e32 v19, vcc, 0, v47, vcc
	v_add_co_u32_e32 v20, vcc, s14, v46
	s_lshl_b32 s10, s2, 10
	s_nop 0
	v_addc_co_u32_e32 v21, vcc, 0, v47, vcc
	s_and_b32 s8, s10, 0x3e000
	s_movk_i32 s16, 0x7000
	v_add_co_u32_e32 v48, vcc, s16, v46
	v_lshl_or_b32 v22, v1, 7, s8
	s_add_i32 s8, s11, 0x4000
	v_addc_co_u32_e32 v49, vcc, 0, v47, vcc
	s_movk_i32 s16, 0x5000
	s_and_b32 s8, s8, 0xc000
	v_add_co_u32_e32 v50, vcc, s16, v46
	s_lshl_b32 s8, s8, 1
	global_load_dwordx4 v[34:37], v[18:19], off offset:2048
	global_load_dwordx4 v[14:17], v[20:21], off offset:2048
	global_load_dwordx4 v[6:9], v[20:21], off offset:1024
	global_load_dwordx4 v[2:5], v[18:19], off offset:1024
	global_load_dwordx4 v[42:45], v[18:19], off offset:3072
	global_load_dwordx4 v[38:41], v[20:21], off offset:3072
	v_addc_co_u32_e32 v51, vcc, 0, v47, vcc
	v_lshl_add_u64 v[72:73], v[74:75], 0, s[8:9]
	v_add_co_u32_e32 v106, vcc, s14, v72
	global_load_dwordx4 v[10:13], v[50:51], off offset:1024
	global_load_dwordx4 v[52:55], v[50:51], off offset:2048
	global_load_dwordx4 v[56:59], v[48:49], off offset:2048
	v_addc_co_u32_e32 v107, vcc, 0, v73, vcc
	v_add_co_u32_e32 v108, vcc, s15, v72
	global_load_dwordx4 v[60:63], v[50:51], off offset:3072
	global_load_dwordx4 v[64:67], v[48:49], off offset:3072
	global_load_ushort v198, v22, s[12:13]
	v_addc_co_u32_e32 v109, vcc, 0, v73, vcc
	global_load_dwordx4 v[68:71], v[108:109], off offset:2048
	global_load_dwordx4 v[78:81], v[106:107], off offset:2048
	global_load_dwordx4 v[82:85], v[106:107], off offset:3072
	global_load_dwordx4 v[86:89], v[108:109], off offset:3072
	s_add_i32 s8, s11, 0x6000
	s_movk_i32 s16, 0x2000
	s_and_b32 s8, s8, 0xe000
	v_add_co_u32_e32 v26, vcc, s16, v46
	s_lshl_b32 s8, s8, 1
	s_nop 0
	v_addc_co_u32_e32 v27, vcc, 0, v47, vcc
	v_lshl_add_u64 v[110:111], v[74:75], 0, s[8:9]
	v_add_co_u32_e32 v112, vcc, s14, v110
	global_load_dwordx4 a[0:3], v[46:47], off
	global_load_dwordx4 a[8:11], v[46:47], off offset:1024
	global_load_dwordx4 a[12:15], v[26:27], off offset:1024
	global_load_dwordx4 a[20:23], v[26:27], off offset:2048
	global_load_dwordx4 a[16:19], v[46:47], off offset:2048
	global_load_dwordx4 a[24:27], v[46:47], off offset:3072
	global_load_dwordx4 a[4:7], v[20:21], off offset:-4096
	global_load_dwordx4 v[22:25], v[20:21], off
	global_load_dwordx4 a[28:31], v[26:27], off offset:3072
	s_nop 0
	global_load_dwordx4 v[18:21], v[18:19], off
	v_addc_co_u32_e32 v113, vcc, 0, v111, vcc
	v_add_co_u32_e32 v114, vcc, s15, v110
	v_lshl_or_b32 v199, v167, 15, v166
	s_nop 0
	v_addc_co_u32_e32 v115, vcc, 0, v111, vcc
	global_load_dwordx4 v[26:29], v[114:115], off offset:1024
	global_load_dwordx4 v[90:93], v[114:115], off offset:2048
	global_load_dwordx4 v[30:33], v[112:113], off offset:1024
	global_load_dwordx4 v[94:97], v[112:113], off offset:2048
	global_load_dwordx4 v[98:101], v[114:115], off offset:3072
	global_load_dwordx4 v[102:105], v[112:113], off offset:3072
	s_movk_i32 s8, 0x6000
	s_load_dwordx2 s[6:7], s[0:1], 0x20
	v_lshlrev_b32_e32 v76, 1, v0
	v_and_b32_e32 v200, 7, v0
	v_and_b32_e32 v128, 64, v76
	v_and_b32_e32 v179, 15, v0
	v_bfe_u32 v201, v0, 4, 1
	v_mov_b32_e32 v196, 0x44444444
	global_load_dwordx4 a[44:47], v[48:49], off offset:-4096
	s_waitcnt vmcnt(31)
	ds_write_b128 v199, v[14:17] offset:1024
	v_add_co_u32_e32 v14, vcc, s8, v46
	s_movk_i32 s8, 0x4000
	s_nop 0
	v_addc_co_u32_e32 v15, vcc, 0, v47, vcc
	s_waitcnt vmcnt(28)
	ds_write_b128 v199, v[42:45] offset:2048
	v_add_co_u32_e32 v42, vcc, s8, v46
	ds_write_b128 v199, v[34:37]
	s_nop 0
	v_addc_co_u32_e32 v43, vcc, 0, v47, vcc
	s_waitcnt vmcnt(27)
	ds_write_b128 v199, v[38:41] offset:3072
	v_add_co_u32_e32 v44, vcc, s16, v72
	global_load_dwordx4 a[36:39], v[14:15], off offset:1024
	global_load_dwordx4 a[32:35], v[42:43], off offset:1024
	global_load_dwordx4 a[48:51], v[42:43], off offset:2048
	global_load_dwordx4 a[52:55], v[14:15], off offset:2048
	global_load_dwordx4 a[60:63], v[14:15], off offset:3072
	global_load_dwordx4 a[40:43], v[50:51], off offset:-4096
	global_load_dwordx4 v[34:37], v[50:51], off
	global_load_dwordx4 v[38:41], v[48:49], off
	s_nop 0
	global_load_dwordx4 v[14:17], v[48:49], off offset:1024
	s_waitcnt vmcnt(34)
	ds_write_b128 v199, v[52:55] offset:4096
	s_waitcnt vmcnt(33)
	ds_write_b128 v199, v[56:59] offset:5120
	v_addc_co_u32_e32 v45, vcc, 0, v73, vcc
	s_xor_b32 s8, s17, 0x8000
	global_load_dwordx4 a[68:71], v[106:107], off offset:-4096
	s_waitcnt vmcnt(33)
	ds_write_b128 v199, v[60:63] offset:6144
	s_waitcnt vmcnt(32)
	ds_write_b128 v199, v[64:67] offset:7168
	v_add_co_u32_e32 v58, vcc, s16, v110
	s_lshl_b32 s8, s8, 1
	global_load_dwordx4 a[56:59], v[42:43], off offset:3072
	global_load_dwordx4 a[64:67], v[72:73], off
	global_load_dwordx4 a[72:75], v[72:73], off offset:1024
	global_load_dwordx4 a[80:83], v[72:73], off offset:2048
	global_load_dwordx4 a[84:87], v[44:45], off offset:2048
	global_load_dwordx4 a[92:95], v[44:45], off offset:3072
	global_load_dwordx4 a[76:79], v[44:45], off offset:1024
	global_load_dwordx4 a[88:91], v[72:73], off offset:3072
	global_load_dwordx4 v[46:49], v[106:107], off
	global_load_dwordx4 v[54:57], v[106:107], off offset:1024
	s_nop 0
	global_load_dwordx4 v[42:45], v[108:109], off
	global_load_dwordx4 v[50:53], v[108:109], off offset:1024
	s_waitcnt vmcnt(42)
	ds_write_b128 v199, v[68:71] offset:8192
	s_waitcnt vmcnt(41)
	ds_write_b128 v199, v[78:81] offset:9216
	s_waitcnt vmcnt(39)
	ds_write_b128 v199, v[86:89] offset:10240
	ds_write_b128 v199, v[82:85] offset:11264
	v_addc_co_u32_e32 v59, vcc, 0, v111, vcc
	v_lshl_add_u64 v[78:79], v[74:75], 0, s[8:9]
	v_add_co_u32_e32 v84, vcc, s14, v78
	global_load_dwordx4 a[96:99], v[110:111], off
	global_load_dwordx4 a[104:107], v[110:111], off offset:1024
	global_load_dwordx4 a[108:111], v[58:59], off offset:1024
	global_load_dwordx4 a[116:119], v[58:59], off offset:2048
	global_load_dwordx4 a[112:115], v[110:111], off offset:2048
	global_load_dwordx4 a[120:123], v[110:111], off offset:3072
	global_load_dwordx4 a[100:103], v[112:113], off offset:-4096
	global_load_dwordx4 v[62:65], v[112:113], off
	global_load_dwordx4 a[124:127], v[58:59], off offset:3072
	s_nop 0
	global_load_dwordx4 v[58:61], v[114:115], off
	v_addc_co_u32_e32 v85, vcc, 0, v79, vcc
	v_add_co_u32_e32 v82, vcc, s15, v78
	s_add_i32 s8, s11, 0xa000
	s_nop 0
	v_addc_co_u32_e32 v83, vcc, 0, v79, vcc
	global_load_dwordx4 v[110:113], v[82:83], off offset:2048
	global_load_dwordx4 v[106:109], v[84:85], off offset:2048
	s_waitcnt vmcnt(39)
	ds_write_b128 v199, v[90:93] offset:12288
	s_waitcnt vmcnt(37)
	ds_write_b128 v199, v[94:97] offset:13312
	s_waitcnt vmcnt(36)
	ds_write_b128 v199, v[98:101] offset:14336
	s_waitcnt vmcnt(35)
	ds_write_b128 v199, v[102:105] offset:15360
	global_load_dwordx4 a[128:131], v[78:79], off
	global_load_dwordx4 a[132:135], v[84:85], off offset:-4096
	global_load_dwordx4 a[136:139], v[78:79], off offset:1024
	global_load_dwordx4 a[144:147], v[78:79], off offset:2048
	global_load_dwordx4 v[102:105], v[82:83], off offset:3072
	global_load_dwordx4 v[98:101], v[84:85], off offset:3072
	s_and_b32 s8, s8, 0xe000
	v_add_co_u32_e32 v80, vcc, s16, v78
	s_lshl_b32 s8, s8, 1
	s_nop 0
	v_addc_co_u32_e32 v81, vcc, 0, v79, vcc
	v_lshl_add_u64 v[122:123], v[74:75], 0, s[8:9]
	v_add_co_u32_e32 v124, vcc, s14, v122
	s_add_i32 s8, s11, 0xc000
	s_nop 0
	v_addc_co_u32_e32 v125, vcc, 0, v123, vcc
	v_add_co_u32_e32 v126, vcc, s15, v122
	s_and_b32 s8, s8, 0xc000
	s_nop 0
	v_addc_co_u32_e32 v127, vcc, 0, v123, vcc
	global_load_dwordx4 v[70:73], v[124:125], off offset:1024
	global_load_dwordx4 v[114:117], v[124:125], off offset:2048
	global_load_dwordx4 v[66:69], v[126:127], off offset:1024
	global_load_dwordx4 v[118:121], v[126:127], off offset:2048
	global_load_dwordx4 a[148:151], v[80:81], off offset:2048
	global_load_dwordx4 a[156:159], v[80:81], off offset:3072
	global_load_dwordx4 v[132:135], v[126:127], off offset:3072
	global_load_dwordx4 v[136:139], v[124:125], off offset:3072
	global_load_dwordx4 a[140:143], v[80:81], off offset:1024
	global_load_dwordx4 a[152:155], v[78:79], off offset:3072
	s_nop 0
	global_load_dwordx4 v[78:81], v[84:85], off
	global_load_dwordx4 v[86:89], v[84:85], off offset:1024
	s_lshl_b32 s8, s8, 1
	v_lshl_add_u64 v[164:165], v[74:75], 0, s[8:9]
	v_add_co_u32_e32 v176, vcc, s14, v164
	s_add_i32 s11, s11, 0xe000
	s_nop 0
	v_addc_co_u32_e32 v177, vcc, 0, v165, vcc
	v_add_co_u32_e32 v184, vcc, s15, v164
	s_and_b32 s8, s11, 0xe000
	s_nop 0
	v_addc_co_u32_e32 v185, vcc, 0, v165, vcc
	global_load_dwordx4 v[140:143], v[184:185], off offset:2048
	global_load_dwordx4 v[144:147], v[176:177], off offset:2048
	global_load_dwordx4 v[148:151], v[176:177], off offset:3072
	global_load_dwordx4 v[152:155], v[184:185], off offset:3072
	s_lshl_b32 s8, s8, 1
	v_lshl_add_u64 v[186:187], v[74:75], 0, s[8:9]
	v_add_co_u32_e32 v188, vcc, s14, v186
	v_and_or_b32 v74, v76, 16, v200
	s_nop 0
	v_addc_co_u32_e32 v189, vcc, 0, v187, vcc
	v_add_co_u32_e32 v190, vcc, s15, v186
	v_lshlrev_b32_e32 v129, 2, v74
	s_nop 0
	v_addc_co_u32_e32 v191, vcc, 0, v187, vcc
	global_load_dwordx4 v[94:97], v[188:189], off offset:1024
	global_load_dwordx4 v[156:159], v[188:189], off offset:2048
	global_load_dwordx4 v[90:93], v[190:191], off offset:1024
	global_load_dwordx4 v[160:163], v[190:191], off offset:2048
	global_load_dwordx4 v[172:175], v[188:189], off offset:3072
	global_load_dwordx4 v[180:183], v[190:191], off offset:3072
	s_waitcnt lgkmcnt(0)
	global_load_dword v131, v129, s[6:7]
	global_load_dwordx4 v[74:77], v[82:83], off
	s_nop 0
	global_load_dwordx4 v[82:85], v[82:83], off offset:1024
	s_waitcnt vmcnt(32)
	ds_write_b128 v199, v[110:113] offset:16384
	s_waitcnt vmcnt(31)
	ds_write_b128 v199, v[106:109] offset:17408
	v_lshlrev_b32_e32 v106, 7, v130
	v_or3_b32 v202, v106, v128, v179
	v_lshlrev_b32_e32 v106, 9, v201
	v_or_b32_e32 v107, 32, v129
	v_or3_b32 v106, v106, s10, v202
	global_load_dword v178, v129, s[6:7] offset:128
	global_load_dword v192, v107, s[6:7] offset:128
	global_load_dword v193, v129, s[6:7] offset:32
	v_ashrrev_i32_e32 v107, 31, v106
	v_lshl_add_u64 v[128:129], v[106:107], 2, s[4:5]
	global_load_dword v171, v[128:129], off
	s_waitcnt vmcnt(30)
	ds_write_b128 v199, v[102:105] offset:18432
	s_waitcnt vmcnt(29)
	ds_write_b128 v199, v[98:101] offset:19456
	v_add_co_u32_e32 v98, vcc, s16, v122
	s_mov_b32 s14, 0x45000000
	s_nop 0
	v_addc_co_u32_e32 v99, vcc, 0, v123, vcc
	global_load_dwordx4 a[160:163], v[122:123], off
	global_load_dwordx4 a[168:171], v[122:123], off offset:1024
	global_load_dwordx4 a[172:175], v[98:99], off offset:1024
	global_load_dwordx4 a[180:183], v[98:99], off offset:2048
	global_load_dwordx4 a[176:179], v[122:123], off offset:2048
	global_load_dwordx4 a[184:187], v[122:123], off offset:3072
	global_load_dword v170, v[128:129], off offset:64
	global_load_dwordx4 a[164:167], v[124:125], off offset:-4096
	global_load_dwordx4 v[102:105], v[124:125], off
	global_load_dwordx4 a[188:191], v[98:99], off offset:3072
	s_nop 0
	global_load_dwordx4 v[98:101], v[126:127], off
	s_waitcnt vmcnt(36)
	ds_write_b128 v199, v[118:121] offset:20480
	ds_write_b128 v199, v[114:117] offset:21504
	global_load_dword v169, v[128:129], off offset:128
	v_add_co_u32_e32 v106, vcc, s16, v164
	s_waitcnt vmcnt(34)
	ds_write_b128 v199, v[132:135] offset:22528
	s_waitcnt vmcnt(33)
	ds_write_b128 v199, v[136:139] offset:23552
	v_addc_co_u32_e32 v107, vcc, 0, v165, vcc
	global_load_dwordx4 a[192:195], v[164:165], off
	global_load_dwordx4 a[196:199], v[176:177], off offset:-4096
	global_load_dwordx4 a[200:203], v[164:165], off offset:1024
	global_load_dwordx4 a[208:211], v[164:165], off offset:2048
	global_load_dwordx4 a[212:215], v[106:107], off offset:2048
	global_load_dwordx4 a[220:223], v[106:107], off offset:3072
	global_load_dwordx4 a[204:207], v[106:107], off offset:1024
	global_load_dwordx4 a[216:219], v[164:165], off offset:3072
	global_load_dwordx4 v[110:113], v[176:177], off
	global_load_dwordx4 v[118:121], v[176:177], off offset:1024
	s_nop 0
	global_load_dwordx4 v[106:109], v[184:185], off
	global_load_dwordx4 v[114:117], v[184:185], off offset:1024
	global_load_dword v168, v[128:129], off offset:192
	v_add_co_u32_e32 v122, vcc, s16, v186
	v_and_b32_e32 v133, 32, v0
	s_nop 0
	v_addc_co_u32_e32 v123, vcc, 0, v187, vcc
	s_waitcnt vmcnt(41)
	ds_write_b128 v199, v[140:143] offset:24576
	s_waitcnt vmcnt(40)
	ds_write_b128 v199, v[144:147] offset:25600
	s_waitcnt vmcnt(38)
	ds_write_b128 v199, v[152:155] offset:26624
	ds_write_b128 v199, v[148:151] offset:27648
	global_load_dwordx4 a[224:227], v[186:187], off
	global_load_dwordx4 a[232:235], v[186:187], off offset:1024
	global_load_dwordx4 a[236:239], v[122:123], off offset:1024
	global_load_dwordx4 a[244:247], v[122:123], off offset:2048
	global_load_dwordx4 a[240:243], v[186:187], off offset:2048
	global_load_dwordx4 a[248:251], v[186:187], off offset:3072
	global_load_dwordx4 a[228:231], v[188:189], off offset:-4096
	global_load_dwordx4 v[126:129], v[188:189], off
	global_load_dwordx4 a[252:255], v[122:123], off offset:3072
	s_nop 0
	global_load_dwordx4 v[122:125], v[190:191], off
	v_lshlrev_b32_e32 v132, 2, v201
	v_lshl_or_b32 v130, v130, 6, v133
	v_lshrrev_b32_e32 v139, 1, v0
	v_and_b32_e32 v203, 24, v139
	s_waitcnt vmcnt(44)
	ds_write_b128 v199, v[160:163] offset:28672
	ds_write_b128 v199, v[156:159] offset:29696
	s_waitcnt vmcnt(42)
	ds_write_b128 v199, v[180:183] offset:30720
	ds_write_b128 v199, v[172:175] offset:31744
	s_waitcnt vmcnt(10) lgkmcnt(0)
	v_lshrrev_b32_e32 v222, 2, v131
	v_and_or_b32 v222, v222, 8, v132
	v_mul_u32_u24_e32 v222, 0x110, v222
	v_and_or_b32 v223, v131, 31, v130
	v_add_lshl_u32 v223, v223, v222, 1
	v_or_b32_e32 v204, 0x20000, v223
	v_lshrrev_b32_e32 v222, 2, v178
	v_and_or_b32 v222, v222, 8, v132
	v_mul_u32_u24_e32 v222, 0x110, v222
	v_and_or_b32 v223, v178, 31, v130
	v_add_lshl_u32 v223, v223, v222, 1
	v_or_b32_e32 v205, 0x20000, v223
	v_lshrrev_b32_e32 v222, 2, v193
	v_and_or_b32 v222, v222, 8, v132
	v_mul_u32_u24_e32 v222, 0x110, v222
	v_and_or_b32 v223, v193, 31, v130
	v_add_lshl_u32 v223, v223, v222, 1
	v_or_b32_e32 v206, 0x20000, v223
	v_lshrrev_b32_e32 v222, 2, v192
	v_and_or_b32 v222, v222, 8, v132
	v_mul_u32_u24_e32 v222, 0x110, v222
	v_and_or_b32 v223, v192, 31, v130
	v_add_lshl_u32 v223, v223, v222, 1
	v_or_b32_e32 v207, 0x20000, v223
	s_movk_i32 s43, 0x110
	v_mad_u32_u24 v224, v179, s43, v203
	v_mov_b32_e32 v225, 0x20000
	v_lshl_or_b32 v224, v224, 1, v225
	s_lshl_b32 s43, s3, 1
	s_add_u32 s52, s43, 0
	s_and_b32 s52, s52, 7
	s_lshl_b32 s52, s52, 6
	s_nop 0
	v_add_u32_e32 v208, s52, v224
	s_add_u32 s52, s43, 1
	s_and_b32 s52, s52, 7
	s_lshl_b32 s52, s52, 6
	s_sub_u32 s52, s52, 64
	s_nop 0
	v_add_u32_e32 v209, s52, v224
	s_add_u32 s52, s43, 2
	s_and_b32 s52, s52, 7
	s_lshl_b32 s52, s52, 6
	s_nop 0
	v_add_u32_e32 v211, s52, v224
	s_add_u32 s52, s43, 3
	s_and_b32 s52, s52, 7
	s_lshl_b32 s52, s52, 6
	s_nop 0
	v_add_u32_e32 v212, s52, v224
	s_add_u32 s52, s43, 4
	s_and_b32 s52, s52, 7
	s_lshl_b32 s52, s52, 6
	s_nop 0
	v_add_u32_e32 v213, s52, v224
	s_add_u32 s52, s43, 5
	s_and_b32 s52, s52, 7
	s_lshl_b32 s52, s52, 6
	s_nop 0
	v_add_u32_e32 v214, s52, v224
	s_add_u32 s52, s43, 6
	s_and_b32 s52, s52, 7
	s_lshl_b32 s52, s52, 6
	s_nop 0
	v_add_u32_e32 v215, s52, v224
	s_add_u32 s52, s43, 7
	s_and_b32 s52, s52, 7
	s_lshl_b32 s52, s52, 6
	s_nop 0
	v_add_u32_e32 v216, s52, v224
	v_and_b32_e32 v225, 8, v0
	v_cmp_eq_u32_e32 vcc, 0, v225
	v_mov_b32_e32 v225, 0xeeeeeeee
	s_nop 1
	v_cndmask_b32_e32 v210, v225, v196, vcc
	v_and_b32_e32 v225, 47, v0
	v_cmp_eq_u32_e64 s[4:5], 0, v225
	v_lshlrev_b32_e32 v225, 4, v167
	v_lshlrev_b32_e32 v226, 3, v201
	s_mov_b32 s52, 0x24400
	v_or3_b32 v218, v225, v226, s52
	s_load_dwordx2 s[6:7], s[0:1], 0x18
	s_lshl_b32 s11, s2, 9
	s_mov_b64 s[22:23], 0
	s_mov_b32 s29, 0
	s_mov_b32 s30, 0
	v_mov_b32_e32 v221, 0
	s_mov_b32 s40, 0x3a000000
	s_mov_b32 s41, 0x34800000
	s_mov_b32 s42, 0x45000000
	v_mov_b32_e32 v217, 0x24480
	v_mov_b64_e32 v[230:231], 0
	v_mov_b64_e32 v[232:233], 0
	v_mov_b64_e32 v[234:235], 0
	v_mov_b64_e32 v[236:237], 0
	v_mov_b64_e32 v[238:239], 0
	v_mov_b64_e32 v[240:241], 0
	v_mov_b64_e32 v[242:243], 0
	v_mov_b64_e32 v[244:245], 0
	ds_write_b128 v217, v[230:233]
	v_mov_b32_e32 v178, 0
	v_fma_mixlo_f16 v131, v178, v238, v171
	v_fma_mixlo_f16 v139, v178, v238, v170
	v_fma_mixlo_f16 v147, v178, v238, v169
	v_fma_mixlo_f16 v155, v178, v238, v168
	v_fma_f32 v130, v178, v238, v171
	v_fma_f32 v138, v178, v238, v170
	v_fma_f32 v146, v178, v238, v169
	v_fma_f32 v154, v178, v238, v168
	v_fma_mix_f32 v130, v130, 1.0, -v131 op_sel_hi:[0,0,1]
	v_fma_mix_f32 v138, v138, 1.0, -v139 op_sel_hi:[0,0,1]
	v_fma_mix_f32 v146, v146, 1.0, -v147 op_sel_hi:[0,0,1]
	v_fma_mix_f32 v154, v154, 1.0, -v155 op_sel_hi:[0,0,1]
	v_fma_mixlo_f16 v133, v130, s42, 0
	v_fma_mixlo_f16 v141, v138, s42, 0
	v_fma_mixlo_f16 v149, v146, s42, 0
	v_fma_mixlo_f16 v157, v154, s42, 0
	v_fma_mix_f32 v130, v130, s42, -v133 op_sel_hi:[0,0,1]
	v_fma_mix_f32 v138, v138, s42, -v141 op_sel_hi:[0,0,1]
	v_fma_mix_f32 v146, v146, s42, -v149 op_sel_hi:[0,0,1]
	v_fma_mix_f32 v154, v154, s42, -v157 op_sel_hi:[0,0,1]
	v_fma_mixlo_f16 v132, v130, s42, 0
	v_fma_mixlo_f16 v140, v138, s42, 0
	v_fma_mixlo_f16 v148, v146, s42, 0
	v_fma_mixlo_f16 v156, v154, s42, 0
	ds_write_b16 v204, v131 offset:8704
	ds_write_b16 v205, v139 offset:8704
	ds_write_b16 v206, v147 offset:8704
	ds_write_b16 v207, v155 offset:8704
	ds_write_b16 v204, v133 offset:9248
	ds_write_b16 v205, v141 offset:9248
	ds_write_b16 v206, v149 offset:9248
	ds_write_b16 v207, v157 offset:9248
	ds_write_b16 v204, v132 offset:9792
	ds_write_b16 v205, v140 offset:9792
	ds_write_b16 v206, v148 offset:9792
	ds_write_b16 v207, v156 offset:9792
	ds_read_b128 v[180:183], v199 offset:0
	s_waitcnt lgkmcnt(6)
	ds_read_b128 v[184:187], v199 offset:1024
	ds_read_b128 v[188:191], v199 offset:4096
	ds_read_b128 v[192:195], v199 offset:5120
	ds_read_b128 v[222:225], v199 offset:8192
	ds_read_b128 v[226:229], v199 offset:9216
	s_waitcnt vmcnt(0)
	s_mov_b32 s53, 1
	s_branch .Lst3_entry
.Lret_f0:
	s_waitcnt lgkmcnt(0)
	v_mov_b32_e32 v173, v166
	v_mov_b32_e32 v172, v167
	v_mov_b32_e32 v175, v176
	v_mov_b32_e32 v174, v177
	s_mov_b32 s52, 0x3a83126f
	v_mov_b32_e32 v248, 0x358637bd
	v_fma_f32 v179, |v171|, s52, v248
	v_fma_f32 v196, |v170|, s52, v248
	v_fma_f32 v197, |v169|, s52, v248
	v_fma_f32 v198, |v168|, s52, v248
	v_rcp_f32_e32 v179, v179
	v_rcp_f32_e32 v196, v196
	v_rcp_f32_e32 v197, v197
	v_rcp_f32_e32 v198, v198
	v_mul_f32_e32 v238, v170, v196
	v_mul_f32_e32 v130, v238, v238
	v_mul_f32_e32 v238, v171, v179
	v_fmac_f32_e32 v130, v238, v238
	v_mul_f32_e32 v238, v169, v197
	v_fmac_f32_e32 v130, v238, v238
	v_mul_f32_e32 v238, v168, v198
	v_fmac_f32_e32 v130, v238, v238
	v_mul_f32_e32 v239, 0x3b000000, v172
	v_mul_f32_e32 v239, v239, v196
	v_mul_f32_e32 v131, v239, v239
	v_mul_f32_e32 v239, 0x3b000000, v173
	v_mul_f32_e32 v239, v239, v179
	v_fmac_f32_e32 v131, v239, v239
	v_mul_f32_e32 v239, 0x3b000000, v175
	v_mul_f32_e32 v239, v239, v197
	v_fmac_f32_e32 v131, v239, v239
	v_mul_f32_e32 v239, 0x3b000000, v174
	v_mul_f32_e32 v239, v239, v198
	v_fmac_f32_e32 v131, v239, v239
	v_add_f32_dpp v130, v130, v130 quad_perm:[1,0,3,2] row_mask:0xf bank_mask:0xf bound_ctrl:1
	s_nop 0
	v_add_f32_dpp v131, v131, v131 quad_perm:[1,0,3,2] row_mask:0xf bank_mask:0xf bound_ctrl:1
	v_add_f32_dpp v130, v130, v130 quad_perm:[2,3,0,1] row_mask:0xf bank_mask:0xf bound_ctrl:1
	s_nop 0
	v_add_f32_dpp v131, v131, v131 quad_perm:[2,3,0,1] row_mask:0xf bank_mask:0xf bound_ctrl:1
	v_add_f32_dpp v130, v130, v130 row_half_mirror row_mask:0xf bank_mask:0xf bound_ctrl:1
	s_nop 0
	v_add_f32_dpp v131, v131, v131 row_half_mirror row_mask:0xf bank_mask:0xf bound_ctrl:1
	v_add_f32_dpp v130, v130, v130 row_mirror row_mask:0xf bank_mask:0xf bound_ctrl:1
	s_nop 0
	v_add_f32_dpp v131, v131, v131 row_mirror row_mask:0xf bank_mask:0xf bound_ctrl:1
	v_mov_b32_e32 v240, v130
	v_mov_b32_e32 v241, v131
	s_nop 0
	v_permlane32_swap_b32_e32 v130, v240
	v_permlane32_swap_b32_e32 v131, v241
	v_add_f32_e32 v130, v130, v240
	v_add_f32_e32 v131, v131, v241
	v_add_u32_e32 v242, 0, v218
	v_lshlrev_b32_e32 v243, 3, v201
	v_or_b32_e32 v243, 0x24400, v243
	s_and_saveexec_b64 s[2:3], s[4:5]
	ds_write_b64 v242, v[130:131]
	s_or_b64 exec, exec, s[2:3]
	s_waitcnt lgkmcnt(0)
	s_barrier
	ds_read_b64 v[134:135], v243 offset:0
	ds_read_b64 v[138:139], v243 offset:16
	ds_read_b64 v[142:143], v243 offset:32
	ds_read_b64 v[146:147], v243 offset:48
	s_waitcnt lgkmcnt(2)
	v_add_f32_e32 v238, v134, v138
	s_waitcnt lgkmcnt(1)
	v_add_f32_e32 v238, v238, v142
	s_waitcnt lgkmcnt(0)
	v_add_f32_e32 v238, v238, v146
	v_add_f32_e32 v239, v135, v139
	v_add_f32_e32 v239, v239, v143
	v_add_f32_e32 v239, v239, v147
	v_mul_f32_e32 v238, 0x3b000000, v238
	v_max_f32_e32 v238, 0xda24260, v238
	v_sqrt_f32_e32 v238, v238
	v_mul_f32_e32 v239, 0x3b000000, v239
	v_max_f32_e32 v239, 0xda24260, v239
	v_sqrt_f32_e32 v239, v239
	s_nop 0
	v_mov_b32_e32 v220, v239
	v_rcp_f32_e32 v240, v239
	v_min_f32_e32 v241, v238, v239
	v_mul_f32_e32 v238, 0x3c23d70a, v238
	v_mul_f32_e32 v238, v238, v240
	s_mov_b32 s52, 0x3727c5ac
	v_cmp_ngt_f32_e32 vcc, s52, v241
	v_mov_b32_e32 v240, 0x358637bd
	s_nop 1
	v_cndmask_b32_e32 v219, v240, v238, vcc
	v_mul_f32_e32 v178, 0x3b000000, v219
	v_fma_mixlo_f16 v131, v178, v173, v171
	v_fma_mixlo_f16 v139, v178, v172, v170
	v_fma_mixlo_f16 v147, v178, v175, v169
	v_fma_mixlo_f16 v155, v178, v174, v168
	v_fma_f32 v130, v178, v173, v171
	v_fma_f32 v138, v178, v172, v170
	v_fma_f32 v146, v178, v175, v169
	v_fma_f32 v154, v178, v174, v168
	v_fma_mix_f32 v130, v130, 1.0, -v131 op_sel_hi:[0,0,1]
	v_fma_mix_f32 v138, v138, 1.0, -v139 op_sel_hi:[0,0,1]
	v_fma_mix_f32 v146, v146, 1.0, -v147 op_sel_hi:[0,0,1]
	v_fma_mix_f32 v154, v154, 1.0, -v155 op_sel_hi:[0,0,1]
	v_fma_mixlo_f16 v133, v130, s42, 0
	v_fma_mixlo_f16 v141, v138, s42, 0
	v_fma_mixlo_f16 v149, v146, s42, 0
	v_fma_mixlo_f16 v157, v154, s42, 0
	v_fma_mix_f32 v130, v130, s42, -v133 op_sel_hi:[0,0,1]
	v_fma_mix_f32 v138, v138, s42, -v141 op_sel_hi:[0,0,1]
	v_fma_mix_f32 v146, v146, s42, -v149 op_sel_hi:[0,0,1]
	v_fma_mix_f32 v154, v154, s42, -v157 op_sel_hi:[0,0,1]
	v_fma_mixlo_f16 v132, v130, s42, 0
	v_fma_mixlo_f16 v140, v138, s42, 0
	v_fma_mixlo_f16 v148, v146, s42, 0
	v_fma_mixlo_f16 v156, v154, s42, 0
	ds_write_b16 v204, v131
	ds_write_b16 v205, v139
	ds_write_b16 v206, v147
	ds_write_b16 v207, v155
	ds_write_b16 v204, v133 offset:544
	ds_write_b16 v205, v141 offset:544
	ds_write_b16 v206, v149 offset:544
	ds_write_b16 v207, v157 offset:544
	ds_write_b16 v204, v132 offset:1088
	ds_write_b16 v205, v140 offset:1088
	ds_write_b16 v206, v148 offset:1088
	ds_write_b16 v207, v156 offset:1088
	s_mov_b32 s53, 2
	s_branch .Lst2_entry
.Lret_f1:
	s_waitcnt lgkmcnt(0)
	v_sub_f32_e32 v238, v163, v172
	v_mul_f32_e32 v238, 0x3b000000, v238
	v_mul_f32_e32 v238, v238, v196
	v_mul_f32_e32 v130, v238, v238
	v_sub_f32_e32 v238, v162, v173
	v_mul_f32_e32 v238, 0x3b000000, v238
	v_mul_f32_e32 v238, v238, v179
	v_fmac_f32_e32 v130, v238, v238
	v_sub_f32_e32 v238, v164, v175
	v_mul_f32_e32 v238, 0x3b000000, v238
	v_mul_f32_e32 v238, v238, v197
	v_fmac_f32_e32 v130, v238, v238
	v_sub_f32_e32 v238, v165, v174
	v_mul_f32_e32 v238, 0x3b000000, v238
	v_mul_f32_e32 v238, v238, v198
	v_fmac_f32_e32 v130, v238, v238
	s_nop 1
	v_add_f32_dpp v130, v130, v130 quad_perm:[1,0,3,2] row_mask:0xf bank_mask:0xf bound_ctrl:1
	s_nop 1
	v_add_f32_dpp v130, v130, v130 quad_perm:[2,3,0,1] row_mask:0xf bank_mask:0xf bound_ctrl:1
	s_nop 1
	v_add_f32_dpp v130, v130, v130 row_half_mirror row_mask:0xf bank_mask:0xf bound_ctrl:1
	s_nop 1
	v_add_f32_dpp v130, v130, v130 row_mirror row_mask:0xf bank_mask:0xf bound_ctrl:1
	v_mov_b32_e32 v240, v130
	s_nop 1
	v_permlane32_swap_b32_e32 v130, v240
	v_add_f32_e32 v130, v130, v240
	v_add_u32_e32 v242, 64, v218
	v_lshlrev_b32_e32 v243, 3, v201
	v_or_b32_e32 v243, 0x24440, v243
	s_and_saveexec_b64 s[2:3], s[4:5]
	ds_write_b32 v242, v130
	s_or_b64 exec, exec, s[2:3]
	s_waitcnt lgkmcnt(0)
	s_barrier
	ds_read2_b32 v[134:135], v243 offset1:4
	ds_read2_b32 v[136:137], v243 offset0:8 offset1:12
	s_waitcnt lgkmcnt(1)
	v_add_f32_e32 v238, v134, v135
	s_waitcnt lgkmcnt(0)
	v_add_f32_e32 v238, v238, v136
	v_add_f32_e32 v238, v238, v137
	v_mul_f32_e32 v238, 0x3b000000, v238
	v_max_f32_e32 v238, 0xda24260, v238
	v_rcp_f32_e32 v240, v219
	v_sqrt_f32_e32 v238, v238
	s_nop 0
	v_mul_f32_e32 v238, v240, v238
	v_max_f32_e32 v241, v220, v238
	v_mul_f32_e32 v242, 0x3a83126f, v219
	v_max_f32_e32 v242, 0x358637bd, v242
	v_max_f32_e32 v243, 0x26901d7d, v241
	v_rcp_f32_e32 v243, v243
	s_nop 0
	v_mul_f32_e32 v243, 0x3c23d70a, v243
	v_log_f32_e32 v243, v243
	s_nop 0
	v_mul_f32_e32 v243, 0x3e4ccccd, v243
	v_exp_f32_e32 v243, v243
	s_mov_b32 s52, 0x26901d7d
	v_cmp_ge_f32_e32 vcc, s52, v241
	s_nop 1
	v_cndmask_b32_e32 v243, v243, v242, vcc
	v_mul_f32_e32 v242, 0x42c80000, v219
	v_min3_f32 v1, v242, v243, 1.0
	s_mov_b32 s53, 0

.Lst2_entry:
	s_waitcnt lgkmcnt(0)
	s_barrier
	ds_read_b128 v[130:133], v208
	ds_read_b128 v[134:137], v209 offset:64
	ds_read_b128 v[138:141], v211
	ds_read_b128 v[142:145], v212
	ds_read_b128 v[146:149], v213
	ds_read_b128 v[150:153], v214
	ds_read_b128 v[154:157], v215
	ds_read_b128 v[158:161], v216
	s_waitcnt lgkmcnt(7)
	v_smfmac_f32_16x16x64_f16 v[230:233], v[130:133], a[16:23], v210
	ds_read_b128 v[238:241], v217
	v_smfmac_f32_16x16x64_f16 v[234:237], v[130:133], v[180:187], v210
	ds_read_b128 v[180:183], v199 offset:12288
	ds_read_b128 v[184:187], v199 offset:13312
	ds_read_b128 v[242:245], v217
	s_waitcnt lgkmcnt(10)
	v_smfmac_f32_16x16x64_f16 v[230:233], v[134:137], a[48:55], v210
	v_mul_f32_e32 v166, 0x3d99999a, v173
	v_smfmac_f32_16x16x64_f16 v[234:237], v[134:137], v[188:195], v210
	ds_read_b128 v[188:191], v199 offset:16384
	ds_read_b128 v[192:195], v199 offset:17408
	v_mul_f32_e32 v167, 0x3d99999a, v172
	s_waitcnt lgkmcnt(11)
	v_smfmac_f32_16x16x64_f16 v[230:233], v[138:141], a[80:87], v210
	v_mul_f32_e32 v176, 0x3d99999a, v175
	v_smfmac_f32_16x16x64_f16 v[234:237], v[138:141], v[222:229], v210
	ds_read_b128 v[222:225], v199 offset:20480
	ds_read_b128 v[226:229], v199 offset:21504
	v_mul_f32_e32 v177, 0x3d99999a, v174
	s_waitcnt lgkmcnt(12)
	v_smfmac_f32_16x16x64_f16 v[230:233], v[142:145], a[112:119], v210
	s_waitcnt lgkmcnt(5)
	v_smfmac_f32_16x16x64_f16 v[234:237], v[142:145], v[180:187], v210
	ds_read_b128 v[180:183], v199 offset:24576
	ds_read_b128 v[184:187], v199 offset:25600
	v_smfmac_f32_16x16x64_f16 v[230:233], v[146:149], a[144:151], v210
	s_waitcnt lgkmcnt(4)
	v_smfmac_f32_16x16x64_f16 v[234:237], v[146:149], v[188:195], v210
	ds_read_b128 v[188:191], v199 offset:28672
	ds_read_b128 v[192:195], v199 offset:29696
	v_smfmac_f32_16x16x64_f16 v[230:233], v[150:153], a[176:183], v210
	s_waitcnt lgkmcnt(4)
	v_smfmac_f32_16x16x64_f16 v[234:237], v[150:153], v[222:229], v210
	ds_read_b128 v[222:225], v199 offset:2048
	ds_read_b128 v[226:229], v199 offset:3072
	v_smfmac_f32_16x16x64_f16 v[230:233], v[154:157], a[208:215], v210
	s_waitcnt lgkmcnt(4)
	v_smfmac_f32_16x16x64_f16 v[234:237], v[154:157], v[180:187], v210
	ds_read_b128 v[180:183], v199 offset:6144
	ds_read_b128 v[184:187], v199 offset:7168
	v_smfmac_f32_16x16x64_f16 v[230:233], v[158:161], a[240:247], v210
	s_waitcnt lgkmcnt(4)
	v_smfmac_f32_16x16x64_f16 v[234:237], v[158:161], v[188:195], v210
	ds_read_b128 v[188:191], v199 offset:10240
	ds_read_b128 v[192:195], v199 offset:11264
	v_smfmac_f32_16x16x64_f16 v[238:241], v[130:133], a[24:31], v210
	s_waitcnt lgkmcnt(4)
	v_smfmac_f32_16x16x64_f16 v[242:245], v[130:133], v[222:229], v210
	ds_read_b128 v[222:225], v199 offset:14336
	ds_read_b128 v[226:229], v199 offset:15360
	v_smfmac_f32_16x16x64_f16 v[238:241], v[134:137], a[56:63], v210
	v_fmac_f32_e32 v230, s40, v231
	v_fmac_f32_e32 v234, s40, v235
	s_waitcnt lgkmcnt(4)
	v_smfmac_f32_16x16x64_f16 v[242:245], v[134:137], v[180:187], v210
	ds_read_b128 v[180:183], v199 offset:18432
	ds_read_b128 v[184:187], v199 offset:19456
	v_fmac_f32_e32 v230, s41, v232
	v_fmac_f32_e32 v234, s41, v236
	v_smfmac_f32_16x16x64_f16 v[238:241], v[138:141], a[88:95], v210
	s_nop 0
	v_permlane32_swap_b32_e32 v230, v234
	v_add_f32_e32 v164, v230, v234
	s_waitcnt lgkmcnt(4)
	v_smfmac_f32_16x16x64_f16 v[242:245], v[138:141], v[188:195], v210
	ds_read_b128 v[188:191], v199 offset:22528
	ds_read_b128 v[192:195], v199 offset:23552
	v_fmac_f32_e32 v176, 0x3e666666, v164
	v_fma_mixlo_f16 v232, v178, v176, v169
	v_smfmac_f32_16x16x64_f16 v[238:241], v[142:145], a[120:127], v210
	v_fma_f32 v231, v178, v176, v169
	v_fma_mix_f32 v231, v231, 1.0, -v232 op_sel_hi:[0,0,1]
	s_waitcnt lgkmcnt(4)
	v_smfmac_f32_16x16x64_f16 v[242:245], v[142:145], v[222:229], v210
	ds_read_b128 v[222:225], v199 offset:26624
	ds_read_b128 v[226:229], v199 offset:27648
	v_fma_mixlo_f16 v235, v231, s42, 0
	v_smfmac_f32_16x16x64_f16 v[238:241], v[146:149], a[152:159], v210
	v_fma_mix_f32 v231, v231, s42, -v235 op_sel_hi:[0,0,1]
	s_waitcnt lgkmcnt(4)
	v_smfmac_f32_16x16x64_f16 v[242:245], v[146:149], v[180:187], v210
	ds_read_b128 v[180:183], v199 offset:30720
	ds_read_b128 v[184:187], v199 offset:31744
	v_fma_mixlo_f16 v233, v231, s42, 0
	v_smfmac_f32_16x16x64_f16 v[238:241], v[150:153], a[184:191], v210
	ds_write_b16 v206, v232 offset:8704
	s_waitcnt lgkmcnt(5)
	v_smfmac_f32_16x16x64_f16 v[242:245], v[150:153], v[188:195], v210
	ds_write_b16 v206, v235 offset:9248
	v_smfmac_f32_16x16x64_f16 v[238:241], v[154:157], a[216:223], v210
	ds_write_b16 v206, v233 offset:9792
	s_waitcnt lgkmcnt(5)
	v_smfmac_f32_16x16x64_f16 v[242:245], v[154:157], v[222:229], v210
	ds_read_b128 v[230:233], v217
	v_smfmac_f32_16x16x64_f16 v[238:241], v[158:161], a[248:255], v210
	ds_read_b128 v[234:237], v217
	s_waitcnt lgkmcnt(5)
	v_smfmac_f32_16x16x64_f16 v[242:245], v[158:161], v[180:187], v210
	s_waitcnt lgkmcnt(1)
	v_smfmac_f32_16x16x64_f16 v[230:233], v[130:133], a[0:7], v210
	s_waitcnt lgkmcnt(0)
	v_smfmac_f32_16x16x64_f16 v[234:237], v[130:133], v[18:25], v210
	v_smfmac_f32_16x16x64_f16 v[230:233], v[134:137], a[40:47], v210
	v_fmac_f32_e32 v238, s40, v239
	v_fmac_f32_e32 v242, s40, v243
	v_smfmac_f32_16x16x64_f16 v[234:237], v[134:137], v[34:41], v210
	v_fmac_f32_e32 v238, s41, v240
	v_fmac_f32_e32 v242, s41, v244
	v_smfmac_f32_16x16x64_f16 v[230:233], v[138:141], a[64:71], v210
	s_nop 0
	v_permlane32_swap_b32_e32 v238, v242
	v_add_f32_e32 v165, v238, v242
	v_smfmac_f32_16x16x64_f16 v[234:237], v[138:141], v[42:49], v210
	v_fmac_f32_e32 v177, 0x3e666666, v165
	v_fma_mixlo_f16 v240, v178, v177, v168
	v_smfmac_f32_16x16x64_f16 v[230:233], v[142:145], a[96:103], v210
	v_fma_f32 v239, v178, v177, v168
	v_fma_mix_f32 v239, v239, 1.0, -v240 op_sel_hi:[0,0,1]
	v_smfmac_f32_16x16x64_f16 v[234:237], v[142:145], v[58:65], v210
	v_fma_mixlo_f16 v243, v239, s42, 0
	v_smfmac_f32_16x16x64_f16 v[230:233], v[146:149], a[128:135], v210
	v_fma_mix_f32 v239, v239, s42, -v243 op_sel_hi:[0,0,1]
	v_smfmac_f32_16x16x64_f16 v[234:237], v[146:149], v[74:81], v210
	v_fma_mixlo_f16 v241, v239, s42, 0
	v_smfmac_f32_16x16x64_f16 v[230:233], v[150:153], a[160:167], v210
	ds_write_b16 v207, v240 offset:8704
	v_smfmac_f32_16x16x64_f16 v[234:237], v[150:153], v[98:105], v210
	ds_write_b16 v207, v243 offset:9248
	v_smfmac_f32_16x16x64_f16 v[230:233], v[154:157], a[192:199], v210
	ds_write_b16 v207, v241 offset:9792
	v_smfmac_f32_16x16x64_f16 v[234:237], v[154:157], v[106:113], v210
	ds_read_b128 v[238:241], v217
	v_smfmac_f32_16x16x64_f16 v[230:233], v[158:161], a[224:231], v210
	ds_read_b128 v[242:245], v217
	v_smfmac_f32_16x16x64_f16 v[234:237], v[158:161], v[122:129], v210
	s_waitcnt lgkmcnt(1)
	v_smfmac_f32_16x16x64_f16 v[238:241], v[130:133], a[8:15], v210
	s_waitcnt lgkmcnt(0)
	v_smfmac_f32_16x16x64_f16 v[242:245], v[130:133], v[2:9], v210
	v_smfmac_f32_16x16x64_f16 v[238:241], v[134:137], a[32:39], v210
	v_fmac_f32_e32 v230, s40, v231
	v_fmac_f32_e32 v234, s40, v235
	v_smfmac_f32_16x16x64_f16 v[242:245], v[134:137], v[10:17], v210
	v_fmac_f32_e32 v230, s41, v232
	v_fmac_f32_e32 v234, s41, v236
	v_smfmac_f32_16x16x64_f16 v[238:241], v[138:141], a[72:79], v210
	s_nop 0
	v_permlane32_swap_b32_e32 v230, v234
	v_add_f32_e32 v162, v230, v234
	v_smfmac_f32_16x16x64_f16 v[242:245], v[138:141], v[50:57], v210
	v_fmac_f32_e32 v166, 0x3e666666, v162
	v_fma_mixlo_f16 v232, v178, v166, v171
	v_smfmac_f32_16x16x64_f16 v[238:241], v[142:145], a[104:111], v210
	v_fma_f32 v231, v178, v166, v171
	v_fma_mix_f32 v231, v231, 1.0, -v232 op_sel_hi:[0,0,1]
	v_smfmac_f32_16x16x64_f16 v[242:245], v[142:145], v[26:33], v210
	v_fma_mixlo_f16 v235, v231, s42, 0
	v_smfmac_f32_16x16x64_f16 v[238:241], v[146:149], a[136:143], v210
	v_fma_mix_f32 v231, v231, s42, -v235 op_sel_hi:[0,0,1]
	v_smfmac_f32_16x16x64_f16 v[242:245], v[146:149], v[82:89], v210
	v_fma_mixlo_f16 v233, v231, s42, 0
	v_smfmac_f32_16x16x64_f16 v[238:241], v[150:153], a[168:175], v210
	ds_write_b16 v204, v232 offset:8704
	v_smfmac_f32_16x16x64_f16 v[242:245], v[150:153], v[66:73], v210
	ds_write_b16 v204, v235 offset:9248
	v_smfmac_f32_16x16x64_f16 v[238:241], v[154:157], a[200:207], v210
	ds_write_b16 v204, v233 offset:9792
	v_smfmac_f32_16x16x64_f16 v[242:245], v[154:157], v[114:121], v210
	ds_read_b128 v[230:233], v217
	v_smfmac_f32_16x16x64_f16 v[238:241], v[158:161], a[232:239], v210
	ds_read_b128 v[234:237], v217
	v_smfmac_f32_16x16x64_f16 v[242:245], v[158:161], v[90:97], v210
	s_nop 5
	v_fmac_f32_e32 v238, s40, v239
	s_nop 0
	v_fmac_f32_e32 v242, s40, v243
	v_fmac_f32_e32 v238, s41, v240
	v_fmac_f32_e32 v242, s41, v244
	s_nop 1
	v_permlane32_swap_b32_e32 v238, v242
	v_add_f32_e32 v163, v238, v242
	v_fmac_f32_e32 v167, 0x3e666666, v163
	v_fma_mixlo_f16 v240, v178, v167, v170
	v_fma_f32 v239, v178, v167, v170
	v_fma_mix_f32 v239, v239, 1.0, -v240 op_sel_hi:[0,0,1]
	v_fma_mixlo_f16 v243, v239, s42, 0
	v_fma_mix_f32 v239, v239, s42, -v243 op_sel_hi:[0,0,1]
	v_fma_mixlo_f16 v241, v239, s42, 0
	ds_write_b16 v205, v240 offset:8704
	ds_write_b16 v205, v243 offset:9248
	ds_write_b16 v205, v241 offset:9792
	ds_read_b128 v[180:183], v199 offset:0
	ds_read_b128 v[184:187], v199 offset:1024
	ds_read_b128 v[188:191], v199 offset:4096
	ds_read_b128 v[192:195], v199 offset:5120
	ds_read_b128 v[222:225], v199 offset:8192
	s_waitcnt lgkmcnt(6)
	ds_read_b128 v[226:229], v199 offset:9216
	s_cmp_eq_u32 s53, 2
	s_cbranch_scc1 .Lret_f1
.Lst3_entry:
	s_waitcnt lgkmcnt(0)
	s_barrier
	ds_read_b128 v[130:133], v208 offset:8704
	ds_read_b128 v[134:137], v209 offset:8768
	ds_read_b128 v[138:141], v211 offset:8704
	ds_read_b128 v[142:145], v212 offset:8704
	ds_read_b128 v[146:149], v213 offset:8704
	ds_read_b128 v[150:153], v214 offset:8704
	ds_read_b128 v[154:157], v215 offset:8704
	ds_read_b128 v[158:161], v216 offset:8704
	s_waitcnt lgkmcnt(7)
	v_smfmac_f32_16x16x64_f16 v[230:233], v[130:133], a[16:23], v210
	ds_read_b128 v[238:241], v217
	v_smfmac_f32_16x16x64_f16 v[234:237], v[130:133], v[180:187], v210
	ds_read_b128 v[180:183], v199 offset:12288
	ds_read_b128 v[184:187], v199 offset:13312
	ds_read_b128 v[242:245], v217
	s_waitcnt lgkmcnt(10)
	v_smfmac_f32_16x16x64_f16 v[230:233], v[134:137], a[48:55], v210
	v_mul_f32_e32 v179, 0x3f7a4fa5, v173
	v_smfmac_f32_16x16x64_f16 v[234:237], v[134:137], v[188:195], v210
	ds_read_b128 v[188:191], v199 offset:16384
	ds_read_b128 v[192:195], v199 offset:17408
	v_fmac_f32_e32 v179, 0xc06eeeef, v162
	s_waitcnt lgkmcnt(11)
	v_smfmac_f32_16x16x64_f16 v[230:233], v[138:141], a[80:87], v210
	v_mul_f32_e32 v196, 0x3f7a4fa5, v172
	v_smfmac_f32_16x16x64_f16 v[234:237], v[138:141], v[222:229], v210
	ds_read_b128 v[222:225], v199 offset:20480
	ds_read_b128 v[226:229], v199 offset:21504
	v_fmac_f32_e32 v196, 0xc06eeeef, v163
	s_waitcnt lgkmcnt(12)
	v_smfmac_f32_16x16x64_f16 v[230:233], v[142:145], a[112:119], v210
	v_mul_f32_e32 v197, 0x3f7a4fa5, v175
	s_waitcnt lgkmcnt(5)
	v_smfmac_f32_16x16x64_f16 v[234:237], v[142:145], v[180:187], v210
	ds_read_b128 v[180:183], v199 offset:24576
	ds_read_b128 v[184:187], v199 offset:25600
	v_fmac_f32_e32 v197, 0xc06eeeef, v164
	v_smfmac_f32_16x16x64_f16 v[230:233], v[146:149], a[144:151], v210
	v_mul_f32_e32 v198, 0x3f7a4fa5, v174
	s_waitcnt lgkmcnt(4)
	v_smfmac_f32_16x16x64_f16 v[234:237], v[146:149], v[188:195], v210
	ds_read_b128 v[188:191], v199 offset:28672
	ds_read_b128 v[192:195], v199 offset:29696
	v_fmac_f32_e32 v198, 0xc06eeeef, v165
	v_smfmac_f32_16x16x64_f16 v[230:233], v[150:153], a[176:183], v210
	s_waitcnt lgkmcnt(4)
	v_smfmac_f32_16x16x64_f16 v[234:237], v[150:153], v[222:229], v210
	ds_read_b128 v[222:225], v199 offset:2048
	ds_read_b128 v[226:229], v199 offset:3072
	v_smfmac_f32_16x16x64_f16 v[230:233], v[154:157], a[208:215], v210
	s_waitcnt lgkmcnt(4)
	v_smfmac_f32_16x16x64_f16 v[234:237], v[154:157], v[180:187], v210
	ds_read_b128 v[180:183], v199 offset:6144
	ds_read_b128 v[184:187], v199 offset:7168
	v_smfmac_f32_16x16x64_f16 v[230:233], v[158:161], a[240:247], v210
	s_waitcnt lgkmcnt(4)
	v_smfmac_f32_16x16x64_f16 v[234:237], v[158:161], v[188:195], v210
	ds_read_b128 v[188:191], v199 offset:10240
	ds_read_b128 v[192:195], v199 offset:11264
	v_smfmac_f32_16x16x64_f16 v[238:241], v[130:133], a[24:31], v210
	s_waitcnt lgkmcnt(4)
	v_smfmac_f32_16x16x64_f16 v[242:245], v[130:133], v[222:229], v210
	ds_read_b128 v[222:225], v199 offset:14336
	ds_read_b128 v[226:229], v199 offset:15360
	v_smfmac_f32_16x16x64_f16 v[238:241], v[134:137], a[56:63], v210
	v_fmac_f32_e32 v230, s40, v231
	v_fmac_f32_e32 v234, s40, v235
	s_waitcnt lgkmcnt(4)
	v_smfmac_f32_16x16x64_f16 v[242:245], v[134:137], v[180:187], v210
	ds_read_b128 v[180:183], v199 offset:18432
	ds_read_b128 v[184:187], v199 offset:19456
	v_fmac_f32_e32 v230, s41, v232
	v_fmac_f32_e32 v234, s41, v236
	v_smfmac_f32_16x16x64_f16 v[238:241], v[138:141], a[88:95], v210
	s_nop 0
	v_permlane32_swap_b32_e32 v230, v234
	v_add_f32_e32 v176, v230, v234
	s_waitcnt lgkmcnt(4)
	v_smfmac_f32_16x16x64_f16 v[242:245], v[138:141], v[188:195], v210
	ds_read_b128 v[188:191], v199 offset:22528
	ds_read_b128 v[192:195], v199 offset:23552
	v_fmac_f32_e32 v197, 0x40638e39, v176
	v_fma_mixlo_f16 v232, v178, v197, v169
	v_smfmac_f32_16x16x64_f16 v[238:241], v[142:145], a[120:127], v210
	v_fma_f32 v231, v178, v197, v169
	v_fma_mix_f32 v231, v231, 1.0, -v232 op_sel_hi:[0,0,1]
	s_waitcnt lgkmcnt(4)
	v_smfmac_f32_16x16x64_f16 v[242:245], v[142:145], v[222:229], v210
	ds_read_b128 v[222:225], v199 offset:26624
	ds_read_b128 v[226:229], v199 offset:27648
	v_fma_mixlo_f16 v235, v231, s42, 0
	v_smfmac_f32_16x16x64_f16 v[238:241], v[146:149], a[152:159], v210
	v_fma_mix_f32 v231, v231, s42, -v235 op_sel_hi:[0,0,1]
	s_waitcnt lgkmcnt(4)
	v_smfmac_f32_16x16x64_f16 v[242:245], v[146:149], v[180:187], v210
	ds_read_b128 v[180:183], v199 offset:30720
	ds_read_b128 v[184:187], v199 offset:31744
	v_fma_mixlo_f16 v233, v231, s42, 0
	v_smfmac_f32_16x16x64_f16 v[238:241], v[150:153], a[184:191], v210
	ds_write_b16 v206, v232
	s_waitcnt lgkmcnt(5)
	v_smfmac_f32_16x16x64_f16 v[242:245], v[150:153], v[188:195], v210
	ds_write_b16 v206, v235 offset:544
	v_smfmac_f32_16x16x64_f16 v[238:241], v[154:157], a[216:223], v210
	ds_write_b16 v206, v233 offset:1088
	s_waitcnt lgkmcnt(5)
	v_smfmac_f32_16x16x64_f16 v[242:245], v[154:157], v[222:229], v210
	ds_read_b128 v[230:233], v217
	v_smfmac_f32_16x16x64_f16 v[238:241], v[158:161], a[248:255], v210
	ds_read_b128 v[234:237], v217
	s_waitcnt lgkmcnt(5)
	v_smfmac_f32_16x16x64_f16 v[242:245], v[158:161], v[180:187], v210
	s_waitcnt lgkmcnt(1)
	v_smfmac_f32_16x16x64_f16 v[230:233], v[130:133], a[0:7], v210
	s_waitcnt lgkmcnt(0)
	v_smfmac_f32_16x16x64_f16 v[234:237], v[130:133], v[18:25], v210
	v_smfmac_f32_16x16x64_f16 v[230:233], v[134:137], a[40:47], v210
	v_fmac_f32_e32 v238, s40, v239
	v_fmac_f32_e32 v242, s40, v243
	v_smfmac_f32_16x16x64_f16 v[234:237], v[134:137], v[34:41], v210
	v_fmac_f32_e32 v238, s41, v240
	v_fmac_f32_e32 v242, s41, v244
	v_smfmac_f32_16x16x64_f16 v[230:233], v[138:141], a[64:71], v210
	s_nop 0
	v_permlane32_swap_b32_e32 v238, v242
	v_add_f32_e32 v177, v238, v242
	v_smfmac_f32_16x16x64_f16 v[234:237], v[138:141], v[42:49], v210
	v_fmac_f32_e32 v198, 0x40638e39, v177
	v_fma_mixlo_f16 v240, v178, v198, v168
	v_smfmac_f32_16x16x64_f16 v[230:233], v[142:145], a[96:103], v210
	v_fma_f32 v239, v178, v198, v168
	v_fma_mix_f32 v239, v239, 1.0, -v240 op_sel_hi:[0,0,1]
	v_smfmac_f32_16x16x64_f16 v[234:237], v[142:145], v[58:65], v210
	v_fma_mixlo_f16 v243, v239, s42, 0
	v_smfmac_f32_16x16x64_f16 v[230:233], v[146:149], a[128:135], v210
	v_fma_mix_f32 v239, v239, s42, -v243 op_sel_hi:[0,0,1]
	v_smfmac_f32_16x16x64_f16 v[234:237], v[146:149], v[74:81], v210
	v_fma_mixlo_f16 v241, v239, s42, 0
	v_smfmac_f32_16x16x64_f16 v[230:233], v[150:153], a[160:167], v210
	ds_write_b16 v207, v240
	v_smfmac_f32_16x16x64_f16 v[234:237], v[150:153], v[98:105], v210
	ds_write_b16 v207, v243 offset:544
	v_smfmac_f32_16x16x64_f16 v[230:233], v[154:157], a[192:199], v210
	ds_write_b16 v207, v241 offset:1088
	v_smfmac_f32_16x16x64_f16 v[234:237], v[154:157], v[106:113], v210
	ds_read_b128 v[238:241], v217
	v_smfmac_f32_16x16x64_f16 v[230:233], v[158:161], a[224:231], v210
	ds_read_b128 v[242:245], v217
	v_smfmac_f32_16x16x64_f16 v[234:237], v[158:161], v[122:129], v210
	s_waitcnt lgkmcnt(1)
	v_smfmac_f32_16x16x64_f16 v[238:241], v[130:133], a[8:15], v210
	s_waitcnt lgkmcnt(0)
	v_smfmac_f32_16x16x64_f16 v[242:245], v[130:133], v[2:9], v210
	v_smfmac_f32_16x16x64_f16 v[238:241], v[134:137], a[32:39], v210
	v_fmac_f32_e32 v230, s40, v231
	v_fmac_f32_e32 v234, s40, v235
	v_smfmac_f32_16x16x64_f16 v[242:245], v[134:137], v[10:17], v210
	v_fmac_f32_e32 v230, s41, v232
	v_fmac_f32_e32 v234, s41, v236
	v_smfmac_f32_16x16x64_f16 v[238:241], v[138:141], a[72:79], v210
	s_nop 0
	v_permlane32_swap_b32_e32 v230, v234
	v_add_f32_e32 v166, v230, v234
	v_smfmac_f32_16x16x64_f16 v[242:245], v[138:141], v[50:57], v210
	v_fmac_f32_e32 v179, 0x40638e39, v166
	v_fma_mixlo_f16 v232, v178, v179, v171
	v_smfmac_f32_16x16x64_f16 v[238:241], v[142:145], a[104:111], v210
	v_fma_f32 v231, v178, v179, v171
	v_fma_mix_f32 v231, v231, 1.0, -v232 op_sel_hi:[0,0,1]
	v_smfmac_f32_16x16x64_f16 v[242:245], v[142:145], v[26:33], v210
	v_fma_mixlo_f16 v235, v231, s42, 0
	v_smfmac_f32_16x16x64_f16 v[238:241], v[146:149], a[136:143], v210
	v_fma_mix_f32 v231, v231, s42, -v235 op_sel_hi:[0,0,1]
	v_smfmac_f32_16x16x64_f16 v[242:245], v[146:149], v[82:89], v210
	v_fma_mixlo_f16 v233, v231, s42, 0
	v_smfmac_f32_16x16x64_f16 v[238:241], v[150:153], a[168:175], v210
	ds_write_b16 v204, v232
	v_smfmac_f32_16x16x64_f16 v[242:245], v[150:153], v[66:73], v210
	ds_write_b16 v204, v235 offset:544
	v_smfmac_f32_16x16x64_f16 v[238:241], v[154:157], a[200:207], v210
	ds_write_b16 v204, v233 offset:1088
	v_smfmac_f32_16x16x64_f16 v[242:245], v[154:157], v[114:121], v210
	ds_read_b128 v[230:233], v217
	v_smfmac_f32_16x16x64_f16 v[238:241], v[158:161], a[232:239], v210
	ds_read_b128 v[234:237], v217
	v_smfmac_f32_16x16x64_f16 v[242:245], v[158:161], v[90:97], v210
	s_nop 5
	v_fmac_f32_e32 v238, s40, v239
	s_nop 0
	v_fmac_f32_e32 v242, s40, v243
	v_fmac_f32_e32 v238, s41, v240
	v_fmac_f32_e32 v242, s41, v244
	s_nop 1
	v_permlane32_swap_b32_e32 v238, v242
	v_add_f32_e32 v167, v238, v242
	v_fmac_f32_e32 v196, 0x40638e39, v167
	v_fma_mixlo_f16 v240, v178, v196, v170
	v_fma_f32 v239, v178, v196, v170
	v_fma_mix_f32 v239, v239, 1.0, -v240 op_sel_hi:[0,0,1]
	v_fma_mixlo_f16 v243, v239, s42, 0
	v_fma_mix_f32 v239, v239, s42, -v243 op_sel_hi:[0,0,1]
	v_fma_mixlo_f16 v241, v239, s42, 0
	ds_write_b16 v205, v240
	ds_write_b16 v205, v243 offset:544
	ds_write_b16 v205, v241 offset:1088
	ds_read_b128 v[180:183], v199 offset:0
	ds_read_b128 v[184:187], v199 offset:1024
	ds_read_b128 v[188:191], v199 offset:4096
	ds_read_b128 v[192:195], v199 offset:5120
	ds_read_b128 v[222:225], v199 offset:8192
	s_waitcnt lgkmcnt(6)
	ds_read_b128 v[226:229], v199 offset:9216
	s_cmp_eq_u32 s53, 1
	s_cbranch_scc1 .Lret_f0
	s_waitcnt lgkmcnt(0)
	s_barrier
	ds_read_b128 v[130:133], v208
	ds_read_b128 v[134:137], v209 offset:64
	ds_read_b128 v[138:141], v211
	ds_read_b128 v[142:145], v212
	ds_read_b128 v[146:149], v213
	ds_read_b128 v[150:153], v214
	ds_read_b128 v[154:157], v215
	ds_read_b128 v[158:161], v216
	s_waitcnt lgkmcnt(7)
	v_smfmac_f32_16x16x64_f16 v[230:233], v[130:133], a[16:23], v210
	ds_read_b128 v[238:241], v217
	v_smfmac_f32_16x16x64_f16 v[234:237], v[130:133], v[180:187], v210
	ds_read_b128 v[180:183], v199 offset:12288
	ds_read_b128 v[184:187], v199 offset:13312
	ds_read_b128 v[242:245], v217
	s_waitcnt lgkmcnt(10)
	v_smfmac_f32_16x16x64_f16 v[230:233], v[134:137], a[48:55], v210
	v_mul_f32_e32 v219, 0x403cf760, v173
	v_smfmac_f32_16x16x64_f16 v[234:237], v[134:137], v[188:195], v210
	ds_read_b128 v[188:191], v199 offset:16384
	ds_read_b128 v[192:195], v199 offset:17408
	v_fmac_f32_e32 v219, 0xc139885f, v162
	s_waitcnt lgkmcnt(11)
	v_smfmac_f32_16x16x64_f16 v[230:233], v[138:141], a[80:87], v210
	v_fmac_f32_e32 v219, 0x411d2a92, v166
	v_smfmac_f32_16x16x64_f16 v[234:237], v[138:141], v[222:229], v210
	ds_read_b128 v[222:225], v199 offset:20480
	ds_read_b128 v[226:229], v199 offset:21504
	v_mul_f32_e32 v220, 0x403cf760, v172
	s_waitcnt lgkmcnt(12)
	v_smfmac_f32_16x16x64_f16 v[230:233], v[142:145], a[112:119], v210
	v_fmac_f32_e32 v220, 0xc139885f, v163
	s_waitcnt lgkmcnt(5)
	v_smfmac_f32_16x16x64_f16 v[234:237], v[142:145], v[180:187], v210
	ds_read_b128 v[180:183], v199 offset:24576
	ds_read_b128 v[184:187], v199 offset:25600
	v_fmac_f32_e32 v220, 0x411d2a92, v167
	v_smfmac_f32_16x16x64_f16 v[230:233], v[146:149], a[144:151], v210
	v_mul_f32_e32 v246, 0x403cf760, v175
	s_waitcnt lgkmcnt(4)
	v_smfmac_f32_16x16x64_f16 v[234:237], v[146:149], v[188:195], v210
	ds_read_b128 v[188:191], v199 offset:28672
	ds_read_b128 v[192:195], v199 offset:29696
	v_fmac_f32_e32 v246, 0xc139885f, v164
	v_smfmac_f32_16x16x64_f16 v[230:233], v[150:153], a[176:183], v210
	v_fmac_f32_e32 v246, 0x411d2a92, v176
	s_waitcnt lgkmcnt(4)
	v_smfmac_f32_16x16x64_f16 v[234:237], v[150:153], v[222:229], v210
	ds_read_b128 v[222:225], v199 offset:2048
	ds_read_b128 v[226:229], v199 offset:3072
	v_mul_f32_e32 v247, 0x403cf760, v174
	v_smfmac_f32_16x16x64_f16 v[230:233], v[154:157], a[208:215], v210
	v_fmac_f32_e32 v247, 0xc139885f, v165
	s_waitcnt lgkmcnt(4)
	v_smfmac_f32_16x16x64_f16 v[234:237], v[154:157], v[180:187], v210
	ds_read_b128 v[180:183], v199 offset:6144
	ds_read_b128 v[184:187], v199 offset:7168
	v_fmac_f32_e32 v247, 0x411d2a92, v177
	v_smfmac_f32_16x16x64_f16 v[230:233], v[158:161], a[240:247], v210
	s_waitcnt lgkmcnt(4)
	v_smfmac_f32_16x16x64_f16 v[234:237], v[158:161], v[188:195], v210
	ds_read_b128 v[188:191], v199 offset:10240
	ds_read_b128 v[192:195], v199 offset:11264
	v_smfmac_f32_16x16x64_f16 v[238:241], v[130:133], a[24:31], v210
	s_waitcnt lgkmcnt(4)
	v_smfmac_f32_16x16x64_f16 v[242:245], v[130:133], v[222:229], v210
	ds_read_b128 v[222:225], v199 offset:14336
	ds_read_b128 v[226:229], v199 offset:15360
	v_smfmac_f32_16x16x64_f16 v[238:241], v[134:137], a[56:63], v210
	v_fmac_f32_e32 v230, s40, v231
	v_fmac_f32_e32 v234, s40, v235
	s_waitcnt lgkmcnt(4)
	v_smfmac_f32_16x16x64_f16 v[242:245], v[134:137], v[180:187], v210
	ds_read_b128 v[180:183], v199 offset:18432
	ds_read_b128 v[184:187], v199 offset:19456
	v_fmac_f32_e32 v230, s41, v232
	v_fmac_f32_e32 v234, s41, v236
	v_smfmac_f32_16x16x64_f16 v[238:241], v[138:141], a[88:95], v210
	s_nop 0
	v_permlane32_swap_b32_e32 v230, v234
	v_add_f32_e32 v197, v230, v234
	s_waitcnt lgkmcnt(4)
	v_smfmac_f32_16x16x64_f16 v[242:245], v[138:141], v[188:195], v210
	ds_read_b128 v[188:191], v199 offset:22528
	ds_read_b128 v[192:195], v199 offset:23552
	v_fmac_f32_e32 v246, 0xbe94e4f6, v197
	v_fma_mixlo_f16 v232, v178, v246, v169
	v_smfmac_f32_16x16x64_f16 v[238:241], v[142:145], a[120:127], v210
	v_fma_f32 v231, v178, v246, v169
	v_fma_mix_f32 v231, v231, 1.0, -v232 op_sel_hi:[0,0,1]
	s_waitcnt lgkmcnt(4)
	v_smfmac_f32_16x16x64_f16 v[242:245], v[142:145], v[222:229], v210
	ds_read_b128 v[222:225], v199 offset:26624
	ds_read_b128 v[226:229], v199 offset:27648
	v_fma_mixlo_f16 v235, v231, s42, 0
	v_smfmac_f32_16x16x64_f16 v[238:241], v[146:149], a[152:159], v210
	v_fma_mix_f32 v231, v231, s42, -v235 op_sel_hi:[0,0,1]
	s_waitcnt lgkmcnt(4)
	v_smfmac_f32_16x16x64_f16 v[242:245], v[146:149], v[180:187], v210
	ds_read_b128 v[180:183], v199 offset:30720
	ds_read_b128 v[184:187], v199 offset:31744
	v_fma_mixlo_f16 v233, v231, s42, 0
	v_smfmac_f32_16x16x64_f16 v[238:241], v[150:153], a[184:191], v210
	ds_write_b16 v206, v232 offset:8704
	s_waitcnt lgkmcnt(5)
	v_smfmac_f32_16x16x64_f16 v[242:245], v[150:153], v[188:195], v210
	ds_write_b16 v206, v235 offset:9248
	v_smfmac_f32_16x16x64_f16 v[238:241], v[154:157], a[216:223], v210
	ds_write_b16 v206, v233 offset:9792
	s_waitcnt lgkmcnt(5)
	v_smfmac_f32_16x16x64_f16 v[242:245], v[154:157], v[222:229], v210
	ds_read_b128 v[230:233], v217
	v_smfmac_f32_16x16x64_f16 v[238:241], v[158:161], a[248:255], v210
	ds_read_b128 v[234:237], v217
	s_waitcnt lgkmcnt(5)
	v_smfmac_f32_16x16x64_f16 v[242:245], v[158:161], v[180:187], v210
	s_waitcnt lgkmcnt(1)
	v_smfmac_f32_16x16x64_f16 v[230:233], v[130:133], a[0:7], v210
	s_waitcnt lgkmcnt(0)
	v_smfmac_f32_16x16x64_f16 v[234:237], v[130:133], v[18:25], v210
	v_smfmac_f32_16x16x64_f16 v[230:233], v[134:137], a[40:47], v210
	v_fmac_f32_e32 v238, s40, v239
	v_fmac_f32_e32 v242, s40, v243
	v_smfmac_f32_16x16x64_f16 v[234:237], v[134:137], v[34:41], v210
	v_fmac_f32_e32 v238, s41, v240
	v_fmac_f32_e32 v242, s41, v244
	v_smfmac_f32_16x16x64_f16 v[230:233], v[138:141], a[64:71], v210
	s_nop 0
	v_permlane32_swap_b32_e32 v238, v242
	v_add_f32_e32 v198, v238, v242
	v_smfmac_f32_16x16x64_f16 v[234:237], v[138:141], v[42:49], v210
	v_fmac_f32_e32 v247, 0xbe94e4f6, v198
	v_fma_mixlo_f16 v240, v178, v247, v168
	v_smfmac_f32_16x16x64_f16 v[230:233], v[142:145], a[96:103], v210
	v_fma_f32 v239, v178, v247, v168
	v_fma_mix_f32 v239, v239, 1.0, -v240 op_sel_hi:[0,0,1]
	v_smfmac_f32_16x16x64_f16 v[234:237], v[142:145], v[58:65], v210
	v_fma_mixlo_f16 v243, v239, s42, 0
	v_smfmac_f32_16x16x64_f16 v[230:233], v[146:149], a[128:135], v210
	v_fma_mix_f32 v239, v239, s42, -v243 op_sel_hi:[0,0,1]
	v_smfmac_f32_16x16x64_f16 v[234:237], v[146:149], v[74:81], v210
	v_fma_mixlo_f16 v241, v239, s42, 0
	v_smfmac_f32_16x16x64_f16 v[230:233], v[150:153], a[160:167], v210
	ds_write_b16 v207, v240 offset:8704
	v_smfmac_f32_16x16x64_f16 v[234:237], v[150:153], v[98:105], v210
	ds_write_b16 v207, v243 offset:9248
	v_smfmac_f32_16x16x64_f16 v[230:233], v[154:157], a[192:199], v210
	ds_write_b16 v207, v241 offset:9792
	v_smfmac_f32_16x16x64_f16 v[234:237], v[154:157], v[106:113], v210
	ds_read_b128 v[238:241], v217
	v_smfmac_f32_16x16x64_f16 v[230:233], v[158:161], a[224:231], v210
	ds_read_b128 v[242:245], v217
	v_smfmac_f32_16x16x64_f16 v[234:237], v[158:161], v[122:129], v210
	s_waitcnt lgkmcnt(1)
	v_smfmac_f32_16x16x64_f16 v[238:241], v[130:133], a[8:15], v210
	s_waitcnt lgkmcnt(0)
	v_smfmac_f32_16x16x64_f16 v[242:245], v[130:133], v[2:9], v210
	v_smfmac_f32_16x16x64_f16 v[238:241], v[134:137], a[32:39], v210
	v_fmac_f32_e32 v230, s40, v231
	v_fmac_f32_e32 v234, s40, v235
	v_smfmac_f32_16x16x64_f16 v[242:245], v[134:137], v[10:17], v210
	v_fmac_f32_e32 v230, s41, v232
	v_fmac_f32_e32 v234, s41, v236
	v_smfmac_f32_16x16x64_f16 v[238:241], v[138:141], a[72:79], v210
	s_nop 0
	v_permlane32_swap_b32_e32 v230, v234
	v_add_f32_e32 v179, v230, v234
	v_smfmac_f32_16x16x64_f16 v[242:245], v[138:141], v[50:57], v210
	v_fmac_f32_e32 v219, 0xbe94e4f6, v179
	v_fma_mixlo_f16 v232, v178, v219, v171
	v_smfmac_f32_16x16x64_f16 v[238:241], v[142:145], a[104:111], v210
	v_fma_f32 v231, v178, v219, v171
	v_fma_mix_f32 v231, v231, 1.0, -v232 op_sel_hi:[0,0,1]
	v_smfmac_f32_16x16x64_f16 v[242:245], v[142:145], v[26:33], v210
	v_fma_mixlo_f16 v235, v231, s42, 0
	v_smfmac_f32_16x16x64_f16 v[238:241], v[146:149], a[136:143], v210
	v_fma_mix_f32 v231, v231, s42, -v235 op_sel_hi:[0,0,1]
	v_smfmac_f32_16x16x64_f16 v[242:245], v[146:149], v[82:89], v210
	v_fma_mixlo_f16 v233, v231, s42, 0
	v_smfmac_f32_16x16x64_f16 v[238:241], v[150:153], a[168:175], v210
	ds_write_b16 v204, v232 offset:8704
	v_smfmac_f32_16x16x64_f16 v[242:245], v[150:153], v[66:73], v210
	ds_write_b16 v204, v235 offset:9248
	v_smfmac_f32_16x16x64_f16 v[238:241], v[154:157], a[200:207], v210
	ds_write_b16 v204, v233 offset:9792
	v_smfmac_f32_16x16x64_f16 v[242:245], v[154:157], v[114:121], v210
	ds_read_b128 v[230:233], v217
	v_smfmac_f32_16x16x64_f16 v[238:241], v[158:161], a[232:239], v210
	ds_read_b128 v[234:237], v217
	v_smfmac_f32_16x16x64_f16 v[242:245], v[158:161], v[90:97], v210
	s_nop 5
	v_fmac_f32_e32 v238, s40, v239
	s_nop 0
	v_fmac_f32_e32 v242, s40, v243
	v_fmac_f32_e32 v238, s41, v240
	v_fmac_f32_e32 v242, s41, v244
	s_nop 1
	v_permlane32_swap_b32_e32 v238, v242
	v_add_f32_e32 v196, v238, v242
	v_fmac_f32_e32 v220, 0xbe94e4f6, v196
	v_fma_mixlo_f16 v240, v178, v220, v170
	v_fma_f32 v239, v178, v220, v170
	v_fma_mix_f32 v239, v239, 1.0, -v240 op_sel_hi:[0,0,1]
	v_fma_mixlo_f16 v243, v239, s42, 0
	v_fma_mix_f32 v239, v239, s42, -v243 op_sel_hi:[0,0,1]
	v_fma_mixlo_f16 v241, v239, s42, 0
	ds_write_b16 v205, v240 offset:8704
	ds_write_b16 v205, v243 offset:9248
	ds_write_b16 v205, v241 offset:9792
	ds_read_b128 v[180:183], v199 offset:0
	ds_read_b128 v[184:187], v199 offset:1024
	ds_read_b128 v[188:191], v199 offset:4096
	ds_read_b128 v[192:195], v199 offset:5120
	ds_read_b128 v[222:225], v199 offset:8192
	s_waitcnt lgkmcnt(6)
	ds_read_b128 v[226:229], v199 offset:9216
	s_waitcnt lgkmcnt(0)
	s_barrier
	ds_read_b128 v[130:133], v208 offset:8704
	ds_read_b128 v[134:137], v209 offset:8768
	ds_read_b128 v[138:141], v211 offset:8704
	ds_read_b128 v[142:145], v212 offset:8704
	ds_read_b128 v[146:149], v213 offset:8704
	ds_read_b128 v[150:153], v214 offset:8704
	ds_read_b128 v[154:157], v215 offset:8704
	ds_read_b128 v[158:161], v216 offset:8704
	s_waitcnt lgkmcnt(7)
	v_smfmac_f32_16x16x64_f16 v[230:233], v[130:133], a[16:23], v210
	ds_read_b128 v[238:241], v217
	ds_read_b128 v[242:245], v217
	v_smfmac_f32_16x16x64_f16 v[234:237], v[130:133], v[180:187], v210
	ds_read_b128 v[180:183], v199 offset:12288
	ds_read_b128 v[184:187], v199 offset:13312
	v_mul_f32_e32 v248, 0x40362960, v173
	v_fmac_f32_e32 v248, 0xc12c1f08, v162
	s_waitcnt lgkmcnt(10)
	v_smfmac_f32_16x16x64_f16 v[230:233], v[134:137], a[48:55], v210
	v_fmac_f32_e32 v248, 0x410e80b5, v166
	v_fmac_f32_e32 v248, 0x3e8e8ba3, v179
	v_smfmac_f32_16x16x64_f16 v[234:237], v[134:137], v[188:195], v210
	ds_read_b128 v[188:191], v199 offset:16384
	ds_read_b128 v[192:195], v199 offset:17408
	v_mul_f32_e32 v249, 0x40362960, v172
	s_waitcnt lgkmcnt(11)
	v_smfmac_f32_16x16x64_f16 v[230:233], v[138:141], a[80:87], v210
	v_fmac_f32_e32 v249, 0xc12c1f08, v163
	v_smfmac_f32_16x16x64_f16 v[234:237], v[138:141], v[222:229], v210
	ds_read_b128 v[222:225], v199 offset:20480
	ds_read_b128 v[226:229], v199 offset:21504
	v_fmac_f32_e32 v249, 0x410e80b5, v167
	s_waitcnt lgkmcnt(12)
	v_smfmac_f32_16x16x64_f16 v[230:233], v[142:145], a[112:119], v210
	v_fmac_f32_e32 v249, 0x3e8e8ba3, v196
	s_waitcnt lgkmcnt(4)
	v_smfmac_f32_16x16x64_f16 v[234:237], v[142:145], v[180:187], v210
	ds_read_b128 v[180:183], v199 offset:24576
	ds_read_b128 v[184:187], v199 offset:25600
	v_mul_f32_e32 v250, 0x40362960, v175
	v_smfmac_f32_16x16x64_f16 v[230:233], v[146:149], a[144:151], v210
	v_fmac_f32_e32 v250, 0xc12c1f08, v164
	s_waitcnt lgkmcnt(4)
	v_smfmac_f32_16x16x64_f16 v[234:237], v[146:149], v[188:195], v210
	ds_read_b128 v[188:191], v199 offset:28672
	ds_read_b128 v[192:195], v199 offset:29696
	v_fmac_f32_e32 v250, 0x410e80b5, v176
	v_smfmac_f32_16x16x64_f16 v[230:233], v[150:153], a[176:183], v210
	v_fmac_f32_e32 v250, 0x3e8e8ba3, v197
	s_waitcnt lgkmcnt(4)
	v_smfmac_f32_16x16x64_f16 v[234:237], v[150:153], v[222:229], v210
	ds_read_b128 v[222:225], v199 offset:2048
	ds_read_b128 v[226:229], v199 offset:3072
	v_mul_f32_e32 v251, 0x40362960, v174
	v_smfmac_f32_16x16x64_f16 v[230:233], v[154:157], a[208:215], v210
	v_fmac_f32_e32 v251, 0xc12c1f08, v165
	s_waitcnt lgkmcnt(4)
	v_smfmac_f32_16x16x64_f16 v[234:237], v[154:157], v[180:187], v210
	ds_read_b128 v[180:183], v199 offset:6144
	ds_read_b128 v[184:187], v199 offset:7168
	v_fmac_f32_e32 v251, 0x410e80b5, v177
	v_smfmac_f32_16x16x64_f16 v[230:233], v[158:161], a[240:247], v210
	v_fmac_f32_e32 v251, 0x3e8e8ba3, v198
	s_waitcnt lgkmcnt(4)
	v_smfmac_f32_16x16x64_f16 v[234:237], v[158:161], v[188:195], v210
	ds_read_b128 v[188:191], v199 offset:10240
	ds_read_b128 v[192:195], v199 offset:11264
	v_smfmac_f32_16x16x64_f16 v[238:241], v[130:133], a[24:31], v210
	s_waitcnt lgkmcnt(4)
	v_smfmac_f32_16x16x64_f16 v[242:245], v[130:133], v[222:229], v210
	ds_read_b128 v[222:225], v199 offset:14336
	ds_read_b128 v[226:229], v199 offset:15360
	v_smfmac_f32_16x16x64_f16 v[238:241], v[134:137], a[56:63], v210
	v_fmac_f32_e32 v230, s40, v231
	v_fmac_f32_e32 v234, s40, v235
	s_waitcnt lgkmcnt(4)
	v_smfmac_f32_16x16x64_f16 v[242:245], v[134:137], v[180:187], v210
	ds_read_b128 v[180:183], v199 offset:18432
	ds_read_b128 v[184:187], v199 offset:19456
	v_fmac_f32_e32 v230, s41, v232
	v_fmac_f32_e32 v234, s41, v236
	v_smfmac_f32_16x16x64_f16 v[238:241], v[138:141], a[88:95], v210
	s_nop 0
	v_permlane32_swap_b32_e32 v230, v234
	v_add_f32_e32 v246, v230, v234
	s_waitcnt lgkmcnt(4)
	v_smfmac_f32_16x16x64_f16 v[242:245], v[138:141], v[188:195], v210
	ds_read_b128 v[188:191], v199 offset:22528
	ds_read_b128 v[192:195], v199 offset:23552
	v_fmac_f32_e32 v250, 0xbe8c0c4c, v246
	v_fma_mixlo_f16 v232, v178, v250, v169
	v_smfmac_f32_16x16x64_f16 v[238:241], v[142:145], a[120:127], v210
	v_fma_f32 v231, v178, v250, v169
	v_fma_mix_f32 v231, v231, 1.0, -v232 op_sel_hi:[0,0,1]
	s_waitcnt lgkmcnt(4)
	v_smfmac_f32_16x16x64_f16 v[242:245], v[142:145], v[222:229], v210
	ds_read_b128 v[222:225], v199 offset:26624
	ds_read_b128 v[226:229], v199 offset:27648
	v_fma_mixlo_f16 v235, v231, s42, 0
	v_smfmac_f32_16x16x64_f16 v[238:241], v[146:149], a[152:159], v210
	v_fma_mix_f32 v231, v231, s42, -v235 op_sel_hi:[0,0,1]
	s_waitcnt lgkmcnt(4)
	v_smfmac_f32_16x16x64_f16 v[242:245], v[146:149], v[180:187], v210
	ds_read_b128 v[180:183], v199 offset:30720
	ds_read_b128 v[184:187], v199 offset:31744
	v_fma_mixlo_f16 v233, v231, s42, 0
	v_smfmac_f32_16x16x64_f16 v[238:241], v[150:153], a[184:191], v210
	ds_write_b16 v206, v232
	s_waitcnt lgkmcnt(5)
	v_smfmac_f32_16x16x64_f16 v[242:245], v[150:153], v[188:195], v210
	ds_write_b16 v206, v235 offset:544
	v_smfmac_f32_16x16x64_f16 v[238:241], v[154:157], a[216:223], v210
	ds_write_b16 v206, v233 offset:1088
	s_waitcnt lgkmcnt(5)
	v_smfmac_f32_16x16x64_f16 v[242:245], v[154:157], v[222:229], v210
	ds_read_b128 v[230:233], v217
	v_smfmac_f32_16x16x64_f16 v[238:241], v[158:161], a[248:255], v210
	ds_read_b128 v[234:237], v217
	s_waitcnt lgkmcnt(5)
	v_smfmac_f32_16x16x64_f16 v[242:245], v[158:161], v[180:187], v210
	s_waitcnt lgkmcnt(1)
	v_smfmac_f32_16x16x64_f16 v[230:233], v[130:133], a[0:7], v210
	s_waitcnt lgkmcnt(0)
	v_smfmac_f32_16x16x64_f16 v[234:237], v[130:133], v[18:25], v210
	v_smfmac_f32_16x16x64_f16 v[230:233], v[134:137], a[40:47], v210
	v_fmac_f32_e32 v238, s40, v239
	v_fmac_f32_e32 v242, s40, v243
	v_smfmac_f32_16x16x64_f16 v[234:237], v[134:137], v[34:41], v210
	v_fmac_f32_e32 v238, s41, v240
	v_fmac_f32_e32 v242, s41, v244
	v_smfmac_f32_16x16x64_f16 v[230:233], v[138:141], a[64:71], v210
	s_nop 0
	v_permlane32_swap_b32_e32 v238, v242
	v_add_f32_e32 v247, v238, v242
	v_smfmac_f32_16x16x64_f16 v[234:237], v[138:141], v[42:49], v210
	v_fmac_f32_e32 v251, 0xbe8c0c4c, v247
	v_fma_mixlo_f16 v240, v178, v251, v168
	v_smfmac_f32_16x16x64_f16 v[230:233], v[142:145], a[96:103], v210
	v_fma_f32 v239, v178, v251, v168
	v_fma_mix_f32 v239, v239, 1.0, -v240 op_sel_hi:[0,0,1]
	v_smfmac_f32_16x16x64_f16 v[234:237], v[142:145], v[58:65], v210
	v_fma_mixlo_f16 v243, v239, s42, 0
	v_smfmac_f32_16x16x64_f16 v[230:233], v[146:149], a[128:135], v210
	v_fma_mix_f32 v239, v239, s42, -v243 op_sel_hi:[0,0,1]
	v_smfmac_f32_16x16x64_f16 v[234:237], v[146:149], v[74:81], v210
	v_fma_mixlo_f16 v241, v239, s42, 0
	v_smfmac_f32_16x16x64_f16 v[230:233], v[150:153], a[160:167], v210
	ds_write_b16 v207, v240
	v_smfmac_f32_16x16x64_f16 v[234:237], v[150:153], v[98:105], v210
	ds_write_b16 v207, v243 offset:544
	v_smfmac_f32_16x16x64_f16 v[230:233], v[154:157], a[192:199], v210
	ds_write_b16 v207, v241 offset:1088
	v_smfmac_f32_16x16x64_f16 v[234:237], v[154:157], v[106:113], v210
	ds_read_b128 v[238:241], v217
	v_smfmac_f32_16x16x64_f16 v[230:233], v[158:161], a[224:231], v210
	ds_read_b128 v[242:245], v217
	v_smfmac_f32_16x16x64_f16 v[234:237], v[158:161], v[122:129], v210
	s_waitcnt lgkmcnt(1)
	v_smfmac_f32_16x16x64_f16 v[238:241], v[130:133], a[8:15], v210
	s_waitcnt lgkmcnt(0)
	v_smfmac_f32_16x16x64_f16 v[242:245], v[130:133], v[2:9], v210
	v_smfmac_f32_16x16x64_f16 v[238:241], v[134:137], a[32:39], v210
	v_fmac_f32_e32 v230, s40, v231
	v_fmac_f32_e32 v234, s40, v235
	v_smfmac_f32_16x16x64_f16 v[242:245], v[134:137], v[10:17], v210
	v_fmac_f32_e32 v230, s41, v232
	v_fmac_f32_e32 v234, s41, v236
	v_smfmac_f32_16x16x64_f16 v[238:241], v[138:141], a[72:79], v210
	s_nop 0
	v_permlane32_swap_b32_e32 v230, v234
	v_add_f32_e32 v219, v230, v234
	v_smfmac_f32_16x16x64_f16 v[242:245], v[138:141], v[50:57], v210
	v_fmac_f32_e32 v248, 0xbe8c0c4c, v219
	v_fma_mixlo_f16 v232, v178, v248, v171
	v_smfmac_f32_16x16x64_f16 v[238:241], v[142:145], a[104:111], v210
	v_fma_f32 v231, v178, v248, v171
	v_fma_mix_f32 v231, v231, 1.0, -v232 op_sel_hi:[0,0,1]
	v_smfmac_f32_16x16x64_f16 v[242:245], v[142:145], v[26:33], v210
	v_fma_mixlo_f16 v235, v231, s42, 0
	v_smfmac_f32_16x16x64_f16 v[238:241], v[146:149], a[136:143], v210
	v_fma_mix_f32 v231, v231, s42, -v235 op_sel_hi:[0,0,1]
	v_smfmac_f32_16x16x64_f16 v[242:245], v[146:149], v[82:89], v210
	v_fma_mixlo_f16 v233, v231, s42, 0
	v_smfmac_f32_16x16x64_f16 v[238:241], v[150:153], a[168:175], v210
	ds_write_b16 v204, v232
	v_smfmac_f32_16x16x64_f16 v[242:245], v[150:153], v[66:73], v210
	ds_write_b16 v204, v235 offset:544
	v_smfmac_f32_16x16x64_f16 v[238:241], v[154:157], a[200:207], v210
	ds_write_b16 v204, v233 offset:1088
	v_smfmac_f32_16x16x64_f16 v[242:245], v[154:157], v[114:121], v210
	ds_read_b128 v[230:233], v217
	v_smfmac_f32_16x16x64_f16 v[238:241], v[158:161], a[232:239], v210
	ds_read_b128 v[234:237], v217
	v_smfmac_f32_16x16x64_f16 v[242:245], v[158:161], v[90:97], v210
	s_nop 5
	v_fmac_f32_e32 v238, s40, v239
	s_nop 0
	v_fmac_f32_e32 v242, s40, v243
	v_fmac_f32_e32 v238, s41, v240
	v_fmac_f32_e32 v242, s41, v244
	s_nop 1
	v_permlane32_swap_b32_e32 v238, v242
	v_add_f32_e32 v220, v238, v242
	v_fmac_f32_e32 v249, 0xbe8c0c4c, v220
	v_fma_mixlo_f16 v240, v178, v249, v170
	v_fma_f32 v239, v178, v249, v170
	v_fma_mix_f32 v239, v239, 1.0, -v240 op_sel_hi:[0,0,1]
	v_fma_mixlo_f16 v243, v239, s42, 0
	v_fma_mix_f32 v239, v239, s42, -v243 op_sel_hi:[0,0,1]
	v_fma_mixlo_f16 v241, v239, s42, 0
	ds_write_b16 v205, v240
	ds_write_b16 v205, v243 offset:544
	ds_write_b16 v205, v241 offset:1088
	ds_read_b128 v[180:183], v199 offset:0
	ds_read_b128 v[184:187], v199 offset:1024
	ds_read_b128 v[188:191], v199 offset:4096
	ds_read_b128 v[192:195], v199 offset:5120
	ds_read_b128 v[222:225], v199 offset:8192
	s_waitcnt lgkmcnt(6)
	ds_read_b128 v[226:229], v199 offset:9216
	s_waitcnt lgkmcnt(0)
	s_barrier
	ds_read_b128 v[130:133], v208
	ds_read_b128 v[134:137], v209 offset:64
	ds_read_b128 v[138:141], v211
	ds_read_b128 v[142:145], v212
	ds_read_b128 v[146:149], v213
	ds_read_b128 v[150:153], v214
	ds_read_b128 v[154:157], v215
	ds_read_b128 v[158:161], v216
	s_waitcnt lgkmcnt(7)
	v_smfmac_f32_16x16x64_f16 v[230:233], v[130:133], a[16:23], v210
	ds_read_b128 v[238:241], v217
	ds_read_b128 v[242:245], v217
	v_smfmac_f32_16x16x64_f16 v[234:237], v[130:133], v[180:187], v210
	ds_read_b128 v[180:183], v199 offset:12288
	ds_read_b128 v[184:187], v199 offset:13312
	v_mul_f32_e32 v252, 0x3dbaaaab, v173
	v_fmac_f32_e32 v252, 0x3ee6024d, v166
	s_waitcnt lgkmcnt(10)
	v_smfmac_f32_16x16x64_f16 v[230:233], v[134:137], a[48:55], v210
	v_fmac_f32_e32 v252, 0x3f26aaab, v179
	v_fmac_f32_e32 v252, 0xbea50e7e, v219
	v_smfmac_f32_16x16x64_f16 v[234:237], v[134:137], v[188:195], v210
	ds_read_b128 v[188:191], v199 offset:16384
	ds_read_b128 v[192:195], v199 offset:17408
	v_mul_f32_e32 v253, 0x3dbaaaab, v172
	s_waitcnt lgkmcnt(11)
	v_smfmac_f32_16x16x64_f16 v[230:233], v[138:141], a[80:87], v210
	v_fmac_f32_e32 v253, 0x3ee6024d, v167
	v_smfmac_f32_16x16x64_f16 v[234:237], v[138:141], v[222:229], v210
	ds_read_b128 v[222:225], v199 offset:20480
	ds_read_b128 v[226:229], v199 offset:21504
	v_fmac_f32_e32 v253, 0x3f26aaab, v196
	s_waitcnt lgkmcnt(12)
	v_smfmac_f32_16x16x64_f16 v[230:233], v[142:145], a[112:119], v210
	v_fmac_f32_e32 v253, 0xbea50e7e, v220
	s_waitcnt lgkmcnt(4)
	v_smfmac_f32_16x16x64_f16 v[234:237], v[142:145], v[180:187], v210
	ds_read_b128 v[180:183], v199 offset:24576
	ds_read_b128 v[184:187], v199 offset:25600
	v_mul_f32_e32 v254, 0x3dbaaaab, v175
	v_smfmac_f32_16x16x64_f16 v[230:233], v[146:149], a[144:151], v210
	v_fmac_f32_e32 v254, 0x3ee6024d, v176
	s_waitcnt lgkmcnt(4)
	v_smfmac_f32_16x16x64_f16 v[234:237], v[146:149], v[188:195], v210
	ds_read_b128 v[188:191], v199 offset:28672
	ds_read_b128 v[192:195], v199 offset:29696
	v_fmac_f32_e32 v254, 0x3f26aaab, v197
	v_smfmac_f32_16x16x64_f16 v[230:233], v[150:153], a[176:183], v210
	v_fmac_f32_e32 v254, 0xbea50e7e, v246
	s_waitcnt lgkmcnt(4)
	v_smfmac_f32_16x16x64_f16 v[234:237], v[150:153], v[222:229], v210
	ds_read_b128 v[222:225], v199 offset:2048
	ds_read_b128 v[226:229], v199 offset:3072
	v_mul_f32_e32 v255, 0x3dbaaaab, v174
	v_smfmac_f32_16x16x64_f16 v[230:233], v[154:157], a[208:215], v210
	v_fmac_f32_e32 v255, 0x3ee6024d, v177
	s_waitcnt lgkmcnt(4)
	v_smfmac_f32_16x16x64_f16 v[234:237], v[154:157], v[180:187], v210
	ds_read_b128 v[180:183], v199 offset:6144
	ds_read_b128 v[184:187], v199 offset:7168
	v_fmac_f32_e32 v255, 0x3f26aaab, v198
	v_smfmac_f32_16x16x64_f16 v[230:233], v[158:161], a[240:247], v210
	v_fmac_f32_e32 v255, 0xbea50e7e, v247
	s_waitcnt lgkmcnt(4)
	v_smfmac_f32_16x16x64_f16 v[234:237], v[158:161], v[188:195], v210
	ds_read_b128 v[188:191], v199 offset:10240
	ds_read_b128 v[192:195], v199 offset:11264
	v_smfmac_f32_16x16x64_f16 v[238:241], v[130:133], a[24:31], v210
	s_waitcnt lgkmcnt(4)
	v_smfmac_f32_16x16x64_f16 v[242:245], v[130:133], v[222:229], v210
	ds_read_b128 v[222:225], v199 offset:14336
	ds_read_b128 v[226:229], v199 offset:15360
	v_smfmac_f32_16x16x64_f16 v[238:241], v[134:137], a[56:63], v210
	v_fmac_f32_e32 v230, s40, v231
	v_fmac_f32_e32 v234, s40, v235
	s_waitcnt lgkmcnt(4)
	v_smfmac_f32_16x16x64_f16 v[242:245], v[134:137], v[180:187], v210
	ds_read_b128 v[180:183], v199 offset:18432
	ds_read_b128 v[184:187], v199 offset:19456
	v_fmac_f32_e32 v230, s41, v232
	v_fmac_f32_e32 v234, s41, v236
	v_smfmac_f32_16x16x64_f16 v[238:241], v[138:141], a[88:95], v210
	s_nop 0
	v_permlane32_swap_b32_e32 v230, v234
	v_add_f32_e32 v250, v230, v234
	s_waitcnt lgkmcnt(4)
	v_smfmac_f32_16x16x64_f16 v[242:245], v[138:141], v[188:195], v210
	ds_read_b128 v[188:191], v199 offset:22528
	ds_read_b128 v[192:195], v199 offset:23552
	v_fmac_f32_e32 v254, 0x3e061862, v250
	v_mov_b32_e32 v236, v254
	v_smfmac_f32_16x16x64_f16 v[238:241], v[142:145], a[120:127], v210
	v_fma_mixlo_f16 v232, v178, v236, v169
	v_fma_f32 v254, v178, v236, v169
	s_waitcnt lgkmcnt(4)
	v_smfmac_f32_16x16x64_f16 v[242:245], v[142:145], v[222:229], v210
	ds_read_b128 v[222:225], v199 offset:26624
	ds_read_b128 v[226:229], v199 offset:27648
	v_fma_mix_f32 v231, v254, 1.0, -v232 op_sel_hi:[0,0,1]
	v_fma_mixlo_f16 v235, v231, s42, 0
	v_smfmac_f32_16x16x64_f16 v[238:241], v[146:149], a[152:159], v210
	v_fma_mix_f32 v231, v231, s42, -v235 op_sel_hi:[0,0,1]
	s_waitcnt lgkmcnt(4)
	v_smfmac_f32_16x16x64_f16 v[242:245], v[146:149], v[180:187], v210
	ds_read_b128 v[180:183], v199 offset:30720
	ds_read_b128 v[184:187], v199 offset:31744
	v_fma_mixlo_f16 v233, v231, s42, 0
	v_smfmac_f32_16x16x64_f16 v[238:241], v[150:153], a[184:191], v210
	ds_write_b16 v206, v232 offset:8704
	s_waitcnt lgkmcnt(5)
	v_smfmac_f32_16x16x64_f16 v[242:245], v[150:153], v[188:195], v210
	ds_write_b16 v206, v235 offset:9248
	v_smfmac_f32_16x16x64_f16 v[238:241], v[154:157], a[216:223], v210
	ds_write_b16 v206, v233 offset:9792
	s_waitcnt lgkmcnt(5)
	v_smfmac_f32_16x16x64_f16 v[242:245], v[154:157], v[222:229], v210
	ds_read_b128 v[230:233], v217
	v_smfmac_f32_16x16x64_f16 v[238:241], v[158:161], a[248:255], v210
	ds_read_b128 v[234:237], v217
	s_waitcnt lgkmcnt(5)
	v_smfmac_f32_16x16x64_f16 v[242:245], v[158:161], v[180:187], v210
	s_waitcnt lgkmcnt(1)
	v_smfmac_f32_16x16x64_f16 v[230:233], v[130:133], a[0:7], v210
	s_waitcnt lgkmcnt(0)
	v_smfmac_f32_16x16x64_f16 v[234:237], v[130:133], v[18:25], v210
	v_smfmac_f32_16x16x64_f16 v[230:233], v[134:137], a[40:47], v210
	v_fmac_f32_e32 v238, s40, v239
	v_fmac_f32_e32 v242, s40, v243
	v_smfmac_f32_16x16x64_f16 v[234:237], v[134:137], v[34:41], v210
	v_fmac_f32_e32 v238, s41, v240
	v_fmac_f32_e32 v242, s41, v244
	v_smfmac_f32_16x16x64_f16 v[230:233], v[138:141], a[64:71], v210
	s_nop 0
	v_permlane32_swap_b32_e32 v238, v242
	v_add_f32_e32 v251, v238, v242
	v_smfmac_f32_16x16x64_f16 v[234:237], v[138:141], v[42:49], v210
	v_fmac_f32_e32 v255, 0x3e061862, v251
	v_mov_b32_e32 v244, v255
	v_smfmac_f32_16x16x64_f16 v[230:233], v[142:145], a[96:103], v210
	v_fma_mixlo_f16 v240, v178, v244, v168
	v_fma_f32 v255, v178, v244, v168
	v_smfmac_f32_16x16x64_f16 v[234:237], v[142:145], v[58:65], v210
	v_fma_mix_f32 v239, v255, 1.0, -v240 op_sel_hi:[0,0,1]
	v_fma_mixlo_f16 v243, v239, s42, 0
	v_smfmac_f32_16x16x64_f16 v[230:233], v[146:149], a[128:135], v210
	v_fma_mix_f32 v239, v239, s42, -v243 op_sel_hi:[0,0,1]
	v_smfmac_f32_16x16x64_f16 v[234:237], v[146:149], v[74:81], v210
	v_fma_mixlo_f16 v241, v239, s42, 0
	v_smfmac_f32_16x16x64_f16 v[230:233], v[150:153], a[160:167], v210
	ds_write_b16 v207, v240 offset:8704
	v_smfmac_f32_16x16x64_f16 v[234:237], v[150:153], v[98:105], v210
	ds_write_b16 v207, v243 offset:9248
	v_smfmac_f32_16x16x64_f16 v[230:233], v[154:157], a[192:199], v210
	ds_write_b16 v207, v241 offset:9792
	v_smfmac_f32_16x16x64_f16 v[234:237], v[154:157], v[106:113], v210
	ds_read_b128 v[238:241], v217
	v_smfmac_f32_16x16x64_f16 v[230:233], v[158:161], a[224:231], v210
	ds_read_b128 v[242:245], v217
	v_smfmac_f32_16x16x64_f16 v[234:237], v[158:161], v[122:129], v210
	s_waitcnt lgkmcnt(1)
	v_smfmac_f32_16x16x64_f16 v[238:241], v[130:133], a[8:15], v210
	s_waitcnt lgkmcnt(0)
	v_smfmac_f32_16x16x64_f16 v[242:245], v[130:133], v[2:9], v210
	v_smfmac_f32_16x16x64_f16 v[238:241], v[134:137], a[32:39], v210
	v_fmac_f32_e32 v230, s40, v231
	v_fmac_f32_e32 v234, s40, v235
	v_smfmac_f32_16x16x64_f16 v[242:245], v[134:137], v[10:17], v210
	v_fmac_f32_e32 v230, s41, v232
	v_fmac_f32_e32 v234, s41, v236
	v_smfmac_f32_16x16x64_f16 v[238:241], v[138:141], a[72:79], v210
	s_nop 0
	v_permlane32_swap_b32_e32 v230, v234
	v_add_f32_e32 v248, v230, v234
	v_smfmac_f32_16x16x64_f16 v[242:245], v[138:141], v[50:57], v210
	v_fmac_f32_e32 v252, 0x3e061862, v248
	v_mov_b32_e32 v236, v252
	v_smfmac_f32_16x16x64_f16 v[238:241], v[142:145], a[104:111], v210
	v_fma_mixlo_f16 v232, v178, v236, v171
	v_fma_f32 v252, v178, v236, v171
	v_smfmac_f32_16x16x64_f16 v[242:245], v[142:145], v[26:33], v210
	v_fma_mix_f32 v231, v252, 1.0, -v232 op_sel_hi:[0,0,1]
	v_fma_mixlo_f16 v235, v231, s42, 0
	v_smfmac_f32_16x16x64_f16 v[238:241], v[146:149], a[136:143], v210
	v_fma_mix_f32 v231, v231, s42, -v235 op_sel_hi:[0,0,1]
	v_smfmac_f32_16x16x64_f16 v[242:245], v[146:149], v[82:89], v210
	v_fma_mixlo_f16 v233, v231, s42, 0
	v_smfmac_f32_16x16x64_f16 v[238:241], v[150:153], a[168:175], v210
	ds_write_b16 v204, v232 offset:8704
	v_smfmac_f32_16x16x64_f16 v[242:245], v[150:153], v[66:73], v210
	ds_write_b16 v204, v235 offset:9248
	v_smfmac_f32_16x16x64_f16 v[238:241], v[154:157], a[200:207], v210
	ds_write_b16 v204, v233 offset:9792
	v_smfmac_f32_16x16x64_f16 v[242:245], v[154:157], v[114:121], v210
	ds_read_b128 v[230:233], v217
	v_smfmac_f32_16x16x64_f16 v[238:241], v[158:161], a[232:239], v210
	ds_read_b128 v[234:237], v217
	v_smfmac_f32_16x16x64_f16 v[242:245], v[158:161], v[90:97], v210
	s_nop 5
	v_fmac_f32_e32 v238, s40, v239
	s_nop 0
	v_fmac_f32_e32 v242, s40, v243
	v_fmac_f32_e32 v238, s41, v240
	v_fmac_f32_e32 v242, s41, v244
	s_nop 1
	v_permlane32_swap_b32_e32 v238, v242
	v_add_f32_e32 v249, v238, v242
	v_fmac_f32_e32 v253, 0x3e061862, v249
	v_mov_b32_e32 v244, v253
	v_fma_mixlo_f16 v240, v178, v244, v170
	v_fma_f32 v253, v178, v244, v170
	v_fma_mix_f32 v239, v253, 1.0, -v240 op_sel_hi:[0,0,1]
	v_fma_mixlo_f16 v243, v239, s42, 0
	v_fma_mix_f32 v239, v239, s42, -v243 op_sel_hi:[0,0,1]
	v_fma_mixlo_f16 v241, v239, s42, 0
	ds_write_b16 v205, v240 offset:8704
	ds_write_b16 v205, v243 offset:9248
	ds_write_b16 v205, v241 offset:9792
	ds_read_b128 v[180:183], v199 offset:0
	ds_read_b128 v[184:187], v199 offset:1024
	ds_read_b128 v[188:191], v199 offset:4096
	ds_read_b128 v[192:195], v199 offset:5120
	ds_read_b128 v[222:225], v199 offset:8192
	s_waitcnt lgkmcnt(6)
	ds_read_b128 v[226:229], v199 offset:9216
	s_waitcnt lgkmcnt(0)
	s_barrier
	ds_read_b128 v[130:133], v208 offset:8704
	ds_read_b128 v[134:137], v209 offset:8768
	ds_read_b128 v[138:141], v211 offset:8704
	ds_read_b128 v[142:145], v212 offset:8704
	ds_read_b128 v[146:149], v213 offset:8704
	ds_read_b128 v[150:153], v214 offset:8704
	ds_read_b128 v[154:157], v215 offset:8704
	ds_read_b128 v[158:161], v216 offset:8704
	s_waitcnt lgkmcnt(7)
	v_smfmac_f32_16x16x64_f16 v[230:233], v[130:133], a[16:23], v210
	ds_read_b128 v[238:241], v217
	ds_read_b128 v[242:245], v217
	v_smfmac_f32_16x16x64_f16 v[234:237], v[130:133], v[180:187], v210
	ds_read_b128 v[180:183], v199 offset:12288
	ds_read_b128 v[184:187], v199 offset:13312
	v_mul_f32_e32 v162, 0x3aa1907f, v173
	v_fmac_f32_e32 v162, 0xbb8b5ad3, v166
	s_waitcnt lgkmcnt(10)
	v_smfmac_f32_16x16x64_f16 v[230:233], v[134:137], a[48:55], v210
	v_fmac_f32_e32 v162, 0x3d177777, v179
	v_fmac_f32_e32 v162, 0xbd50568f, v219
	v_smfmac_f32_16x16x64_f16 v[234:237], v[134:137], v[188:195], v210
	ds_read_b128 v[188:191], v199 offset:16384
	ds_read_b128 v[192:195], v199 offset:17408
	v_fmac_f32_e32 v162, 0x3d2ba454, v248
	v_mul_f32_e32 v163, 0x3aa1907f, v172
	s_waitcnt lgkmcnt(11)
	v_smfmac_f32_16x16x64_f16 v[230:233], v[138:141], a[80:87], v210
	v_fmac_f32_e32 v163, 0xbb8b5ad3, v167
	v_fmac_f32_e32 v163, 0x3d177777, v196
	v_smfmac_f32_16x16x64_f16 v[234:237], v[138:141], v[222:229], v210
	ds_read_b128 v[222:225], v199 offset:20480
	ds_read_b128 v[226:229], v199 offset:21504
	v_fmac_f32_e32 v163, 0xbd50568f, v220
	v_fmac_f32_e32 v163, 0x3d2ba454, v249
	s_waitcnt lgkmcnt(12)
	v_smfmac_f32_16x16x64_f16 v[230:233], v[142:145], a[112:119], v210
	v_mul_f32_e32 v164, 0x3aa1907f, v175
	v_fmac_f32_e32 v164, 0xbb8b5ad3, v176
	s_waitcnt lgkmcnt(4)
	v_smfmac_f32_16x16x64_f16 v[234:237], v[142:145], v[180:187], v210
	ds_read_b128 v[180:183], v199 offset:24576
	ds_read_b128 v[184:187], v199 offset:25600
	v_fmac_f32_e32 v164, 0x3d177777, v197
	v_fmac_f32_e32 v164, 0xbd50568f, v246
	v_smfmac_f32_16x16x64_f16 v[230:233], v[146:149], a[144:151], v210
	v_fmac_f32_e32 v164, 0x3d2ba454, v250
	v_mul_f32_e32 v165, 0x3aa1907f, v174
	s_waitcnt lgkmcnt(4)
	v_smfmac_f32_16x16x64_f16 v[234:237], v[146:149], v[188:195], v210
	ds_read_b128 v[188:191], v199 offset:28672
	ds_read_b128 v[192:195], v199 offset:29696
	v_fmac_f32_e32 v165, 0xbb8b5ad3, v177
	v_fmac_f32_e32 v165, 0x3d177777, v198
	v_smfmac_f32_16x16x64_f16 v[230:233], v[150:153], a[176:183], v210
	v_fmac_f32_e32 v165, 0xbd50568f, v247
	v_fmac_f32_e32 v165, 0x3d2ba454, v251
	s_waitcnt lgkmcnt(4)
	v_smfmac_f32_16x16x64_f16 v[234:237], v[150:153], v[222:229], v210
	ds_read_b128 v[222:225], v199 offset:2048
	ds_read_b128 v[226:229], v199 offset:3072
	v_max_f32_e64 v179, |v171|, |v252|
	v_mov_b32_e32 v248, 0x358637bd
	v_smfmac_f32_16x16x64_f16 v[230:233], v[154:157], a[208:215], v210
	v_fmac_f32_e32 v248, 0x3a83126f, v179
	v_rcp_f32_e32 v179, v248
	s_waitcnt lgkmcnt(4)
	v_smfmac_f32_16x16x64_f16 v[234:237], v[154:157], v[180:187], v210
	ds_read_b128 v[180:183], v199 offset:6144
	ds_read_b128 v[184:187], v199 offset:7168
	v_max_f32_e64 v196, |v170|, |v253|
	v_mov_b32_e32 v249, 0x358637bd
	v_smfmac_f32_16x16x64_f16 v[230:233], v[158:161], a[240:247], v210
	v_fmac_f32_e32 v249, 0x3a83126f, v196
	v_rcp_f32_e32 v196, v249
	s_waitcnt lgkmcnt(4)
	v_smfmac_f32_16x16x64_f16 v[234:237], v[158:161], v[188:195], v210
	ds_read_b128 v[188:191], v199 offset:10240
	ds_read_b128 v[192:195], v199 offset:11264
	v_max_f32_e64 v197, |v169|, |v254|
	v_mov_b32_e32 v250, 0x358637bd
	v_fmac_f32_e32 v250, 0x3a83126f, v197
	v_rcp_f32_e32 v197, v250
	v_max_f32_e64 v198, |v168|, |v255|
	v_mov_b32_e32 v251, 0x358637bd
	v_fmac_f32_e32 v251, 0x3a83126f, v198
	v_rcp_f32_e32 v198, v251
	v_smfmac_f32_16x16x64_f16 v[238:241], v[130:133], a[24:31], v210
	s_waitcnt lgkmcnt(4)
	v_smfmac_f32_16x16x64_f16 v[242:245], v[130:133], v[222:229], v210
	ds_read_b128 v[222:225], v199 offset:14336
	ds_read_b128 v[226:229], v199 offset:15360
	v_smfmac_f32_16x16x64_f16 v[238:241], v[134:137], a[56:63], v210
	v_fmac_f32_e32 v230, s40, v231
	s_waitcnt lgkmcnt(4)
	v_smfmac_f32_16x16x64_f16 v[242:245], v[134:137], v[180:187], v210
	ds_read_b128 v[180:183], v199 offset:18432
	ds_read_b128 v[184:187], v199 offset:19456
	v_fmac_f32_e32 v234, s40, v235
	v_smfmac_f32_16x16x64_f16 v[238:241], v[138:141], a[88:95], v210
	v_fmac_f32_e32 v230, s41, v232
	s_waitcnt lgkmcnt(4)
	v_smfmac_f32_16x16x64_f16 v[242:245], v[138:141], v[188:195], v210
	ds_read_b128 v[188:191], v199 offset:22528
	ds_read_b128 v[192:195], v199 offset:23552
	v_fmac_f32_e32 v234, s41, v236
	v_smfmac_f32_16x16x64_f16 v[238:241], v[142:145], a[120:127], v210
	s_nop 0
	v_permlane32_swap_b32_e32 v230, v234
	s_waitcnt lgkmcnt(4)
	v_smfmac_f32_16x16x64_f16 v[242:245], v[142:145], v[222:229], v210
	ds_read_b128 v[222:225], v199 offset:26624
	ds_read_b128 v[226:229], v199 offset:27648
	v_add_f32_e32 v176, v230, v234
	v_smfmac_f32_16x16x64_f16 v[238:241], v[146:149], a[152:159], v210
	v_fmac_f32_e32 v164, 0xbccccccd, v176
	s_waitcnt lgkmcnt(4)
	v_smfmac_f32_16x16x64_f16 v[242:245], v[146:149], v[180:187], v210
	ds_read_b128 v[180:183], v199 offset:30720
	ds_read_b128 v[184:187], v199 offset:31744
	v_mul_f32_e32 v231, v178, v164
	v_smfmac_f32_16x16x64_f16 v[238:241], v[150:153], a[184:191], v210
	v_mul_f32_e32 v231, v231, v197
	s_waitcnt lgkmcnt(4)
	v_smfmac_f32_16x16x64_f16 v[242:245], v[150:153], v[188:195], v210
	v_mul_f32_e32 v219, v231, v231
	v_smfmac_f32_16x16x64_f16 v[238:241], v[154:157], a[216:223], v210
	ds_read_b128 v[230:233], v217
	s_waitcnt lgkmcnt(3)
	v_smfmac_f32_16x16x64_f16 v[242:245], v[154:157], v[222:229], v210
	ds_read_b128 v[234:237], v217
	v_smfmac_f32_16x16x64_f16 v[238:241], v[158:161], a[248:255], v210
	s_waitcnt lgkmcnt(2)
	v_smfmac_f32_16x16x64_f16 v[242:245], v[158:161], v[180:187], v210
	s_waitcnt lgkmcnt(1)
	v_smfmac_f32_16x16x64_f16 v[230:233], v[130:133], a[0:7], v210
	s_waitcnt lgkmcnt(0)
	v_smfmac_f32_16x16x64_f16 v[234:237], v[130:133], v[18:25], v210
	v_smfmac_f32_16x16x64_f16 v[230:233], v[134:137], a[40:47], v210
	v_fmac_f32_e32 v238, s40, v239
	v_smfmac_f32_16x16x64_f16 v[234:237], v[134:137], v[34:41], v210
	v_fmac_f32_e32 v242, s40, v243
	v_smfmac_f32_16x16x64_f16 v[230:233], v[138:141], a[64:71], v210
	v_fmac_f32_e32 v238, s41, v240
	v_smfmac_f32_16x16x64_f16 v[234:237], v[138:141], v[42:49], v210
	v_fmac_f32_e32 v242, s41, v244
	v_smfmac_f32_16x16x64_f16 v[230:233], v[142:145], a[96:103], v210
	s_nop 0
	v_permlane32_swap_b32_e32 v238, v242
	v_smfmac_f32_16x16x64_f16 v[234:237], v[142:145], v[58:65], v210
	v_add_f32_e32 v177, v238, v242
	v_smfmac_f32_16x16x64_f16 v[230:233], v[146:149], a[128:135], v210
	v_fmac_f32_e32 v165, 0xbccccccd, v177
	v_smfmac_f32_16x16x64_f16 v[234:237], v[146:149], v[74:81], v210
	v_mul_f32_e32 v239, v178, v165
	v_smfmac_f32_16x16x64_f16 v[230:233], v[150:153], a[160:167], v210
	v_mul_f32_e32 v239, v239, v198
	v_smfmac_f32_16x16x64_f16 v[234:237], v[150:153], v[98:105], v210
	v_fmac_f32_e32 v219, v239, v239
	v_smfmac_f32_16x16x64_f16 v[230:233], v[154:157], a[192:199], v210
	ds_read_b128 v[238:241], v217
	v_smfmac_f32_16x16x64_f16 v[234:237], v[154:157], v[106:113], v210
	ds_read_b128 v[242:245], v217
	v_smfmac_f32_16x16x64_f16 v[230:233], v[158:161], a[224:231], v210
	v_smfmac_f32_16x16x64_f16 v[234:237], v[158:161], v[122:129], v210
	s_waitcnt lgkmcnt(1)
	v_smfmac_f32_16x16x64_f16 v[238:241], v[130:133], a[8:15], v210
	s_waitcnt lgkmcnt(0)
	v_smfmac_f32_16x16x64_f16 v[242:245], v[130:133], v[2:9], v210
	v_smfmac_f32_16x16x64_f16 v[238:241], v[134:137], a[32:39], v210
	v_fmac_f32_e32 v230, s40, v231
	v_smfmac_f32_16x16x64_f16 v[242:245], v[134:137], v[10:17], v210
	v_fmac_f32_e32 v234, s40, v235
	v_smfmac_f32_16x16x64_f16 v[238:241], v[138:141], a[72:79], v210
	v_fmac_f32_e32 v230, s41, v232
	v_smfmac_f32_16x16x64_f16 v[242:245], v[138:141], v[50:57], v210
	v_fmac_f32_e32 v234, s41, v236
	v_smfmac_f32_16x16x64_f16 v[238:241], v[142:145], a[104:111], v210
	s_nop 0
	v_permlane32_swap_b32_e32 v230, v234
	v_smfmac_f32_16x16x64_f16 v[242:245], v[142:145], v[26:33], v210
	v_add_f32_e32 v166, v230, v234
	v_smfmac_f32_16x16x64_f16 v[238:241], v[146:149], a[136:143], v210
	v_fmac_f32_e32 v162, 0xbccccccd, v166
	v_smfmac_f32_16x16x64_f16 v[242:245], v[146:149], v[82:89], v210
	v_mul_f32_e32 v231, v178, v162
	v_smfmac_f32_16x16x64_f16 v[238:241], v[150:153], a[168:175], v210
	v_mul_f32_e32 v231, v231, v179
	v_smfmac_f32_16x16x64_f16 v[242:245], v[150:153], v[66:73], v210
	v_fmac_f32_e32 v219, v231, v231
	v_smfmac_f32_16x16x64_f16 v[238:241], v[154:157], a[200:207], v210
	ds_read_b128 v[230:233], v217
	v_smfmac_f32_16x16x64_f16 v[242:245], v[154:157], v[114:121], v210
	ds_read_b128 v[234:237], v217
	v_smfmac_f32_16x16x64_f16 v[238:241], v[158:161], a[232:239], v210
	v_smfmac_f32_16x16x64_f16 v[242:245], v[158:161], v[90:97], v210
	s_nop 6
	v_fmac_f32_e32 v238, s40, v239
	v_fmac_f32_e32 v242, s40, v243
	v_fmac_f32_e32 v238, s41, v240
	v_fmac_f32_e32 v242, s41, v244
	s_nop 1
	v_permlane32_swap_b32_e32 v238, v242
	v_add_f32_e32 v167, v238, v242
	v_fmac_f32_e32 v163, 0xbccccccd, v167
	v_mul_f32_e32 v239, v178, v163
	v_mul_f32_e32 v239, v239, v196
	v_fmac_f32_e32 v219, v239, v239
	ds_read_b128 v[180:183], v199 offset:0
	ds_read_b128 v[184:187], v199 offset:1024
	ds_read_b128 v[188:191], v199 offset:4096
	ds_read_b128 v[192:195], v199 offset:5120
	ds_read_b128 v[222:225], v199 offset:8192
	ds_read_b128 v[226:229], v199 offset:9216
	v_add_f32_dpp v238, v219, v219 quad_perm:[1,0,3,2] row_mask:0xf bank_mask:0xf bound_ctrl:1
	s_nop 1
	v_add_f32_dpp v238, v238, v238 quad_perm:[2,3,0,1] row_mask:0xf bank_mask:0xf bound_ctrl:1
	s_nop 1
	v_add_f32_dpp v238, v238, v238 row_half_mirror row_mask:0xf bank_mask:0xf bound_ctrl:1
	s_nop 1
	v_add_f32_dpp v238, v238, v238 row_mirror row_mask:0xf bank_mask:0xf bound_ctrl:1
	v_mov_b32_e32 v239, v238
	s_nop 1
	v_permlane32_swap_b32_e32 v238, v239
	v_add_f32_e32 v238, v238, v239
	v_lshl_add_u32 v240, s29, 6, v218
	v_lshlrev_b32_e32 v241, 3, v201
	v_or_b32_e32 v241, 0x24400, v241
	v_lshl_add_u32 v241, s29, 6, v241
	s_and_saveexec_b64 s[2:3], s[4:5]
	ds_write_b32 v240, v238
	s_or_b64 exec, exec, s[2:3]
	s_waitcnt lgkmcnt(0)
	s_barrier
	ds_read2_b32 v[130:131], v241 offset1:4
	ds_read2_b32 v[132:133], v241 offset0:8 offset1:12
	s_waitcnt lgkmcnt(1)
	v_add_f32_e32 v238, v130, v131
	s_waitcnt lgkmcnt(0)
	v_add_f32_e32 v238, v238, v132
	v_add_f32_e32 v238, v238, v133
	v_mul_f32_e32 v238, 0x3b000000, v238
	v_max_f32_e32 v238, 0xda24260, v238
	v_sqrt_f32_e32 v238, v238
	s_nop 0
	v_cmp_ngt_f32_e64 s[2:3], 1.0, v238
	v_cmp_gt_f32_e32 vcc, 1.0, v238
	v_log_f32_e32 v239, v238
	v_mul_f32_e32 v241, 0x44000000, v178
	s_and_saveexec_b64 s[26:27], vcc
	v_add_f32_e32 v221, v221, v241
	v_mov_b32_e32 v171, v252
	v_mov_b32_e32 v173, v166
	v_mov_b32_e32 v170, v253
	v_mov_b32_e32 v172, v167
	v_mov_b32_e32 v169, v254
	v_mov_b32_e32 v175, v176
	v_mov_b32_e32 v168, v255
	v_mov_b32_e32 v174, v177
	s_or_b64 exec, exec, s[26:27]
	v_mov_b32_e32 v240, 0x41200000
	s_nop 0
	v_cndmask_b32_e64 v240, v240, 1.0, s[22:23]
	s_xor_b32 s29, s29, 1
	s_add_i32 s30, s30, 1
	v_mul_f32_e32 v239, 0xbe4ccccd, v239
	v_exp_f32_e32 v239, v239
	s_nop 0
	v_mul_f32_e32 v239, 0x3f666666, v239
	v_min_f32_e32 v240, v239, v240
	v_max_f32_e32 v239, 0x3e4ccccd, v239
	v_cndmask_b32_e64 v239, v240, v239, s[2:3]
	v_mul_f32_e32 v1, v241, v239
	s_mov_b64 s[22:23], s[2:3]
	s_branch .Lrk_top
